# P6 EpiGate epilogue hand-rescheduled (all gate loads up-front, counted waits) + tile-contiguous gate buffer layout
# speedup vs baseline: 1.0514x; 1.0514x over previous
; __device__ __forceinline__ unsigned cvt_pk_bf16(float lo, float hi) { unsigned r; asm volatile("v_cvt_pk_bf16_f32 %0, %1, %2" : "=v"(r) : "v"(lo), "v"(hi)); return r; }
;     __device__ __forceinline__ void operator()(const f32x4 (&acc)[2][2][4][2], const pg8::Unit& u, int wr, int wc, int fr, int fq_in) const {
;     ...
;         } else if (pn < 60) {
;             const int col0 = (pn - 44) * 256 + wc * 32 + 8 * fq;
; #pragma unroll
;             for (int ai = 0; ai < 2; ++ai)
; #pragma unroll
;                 for (int m = 0; m < 4; ++m) { bf16* rowp = Gt + (size_t)(row0 + ai * 128 + m * 16) * (2 * D) + col0;
; #pragma unroll
;                     for (int bj = 0; bj < 2; ++bj) { const f32x4 v0 = acc[ai][bj][m][0], v1 = acc[ai][bj][m][1];
;                         u32x4 w; w.x = pg8::cvt_pk_bf16(v0[0], v0[1]); w.y = pg8::cvt_pk_bf16(v0[2], v0[3]); w.z = pg8::cvt_pk_bf16(v1[0], v1[1]); w.w = pg8::cvt_pk_bf16(v1[2], v1[3]);
;                         *(u32x4*)(rowp + bj * 128) = w; } }
.LBB0_471:
	s_andn2_b64 vcc, exec, s[0:1]
	s_cbranch_vccnz .LBB0_473
	s_lshl_b32 s0, s62, 4
	s_add_i32 s0, s0, s64
	s_add_i32 s0, s0, 0xffffffd4
	s_lshl_b32 s0, s0, 17
	v_lshl_add_u32 v130, v0, 4, s0
	v_ashrrev_i32_e32 v179, 31, v178
	v_cvt_pk_bf16_f32 v132, v126, v127
	v_cvt_pk_bf16_f32 v133, v128, v129
	v_cvt_pk_bf16_f32 v134, v122, v123
	v_cvt_pk_bf16_f32 v135, v124, v125
	global_store_dwordx4 v130, v[132:135], s[36:37]
	s_nop 1
	v_cvt_pk_bf16_f32 v132, v114, v115
	v_cvt_pk_bf16_f32 v133, v116, v117
	v_cvt_pk_bf16_f32 v134, v106, v107
	v_cvt_pk_bf16_f32 v135, v108, v109
	v_add_u32_e32 v131, 0x2000, v130
	global_store_dwordx4 v131, v[132:135], s[36:37]
	s_nop 1
	v_cvt_pk_bf16_f32 v132, v118, v119
	v_cvt_pk_bf16_f32 v133, v120, v121
	v_cvt_pk_bf16_f32 v134, v110, v111
	v_cvt_pk_bf16_f32 v135, v112, v113
	v_add_u32_e32 v131, 0x4000, v130
	global_store_dwordx4 v131, v[132:135], s[36:37]
	s_nop 1
	v_cvt_pk_bf16_f32 v132, v98, v99
	v_cvt_pk_bf16_f32 v133, v100, v101
	v_cvt_pk_bf16_f32 v134, v90, v91
	v_cvt_pk_bf16_f32 v135, v92, v93
	v_add_u32_e32 v131, 0x6000, v130
	global_store_dwordx4 v131, v[132:135], s[36:37]
	s_nop 1
	v_cvt_pk_bf16_f32 v132, v102, v103
	v_cvt_pk_bf16_f32 v133, v104, v105
	v_cvt_pk_bf16_f32 v134, v94, v95
	v_cvt_pk_bf16_f32 v135, v96, v97
	v_add_u32_e32 v131, 0x8000, v130
	global_store_dwordx4 v131, v[132:135], s[36:37]
	s_nop 1
	v_cvt_pk_bf16_f32 v132, v82, v83
	v_cvt_pk_bf16_f32 v133, v84, v85
	v_cvt_pk_bf16_f32 v134, v74, v75
	v_cvt_pk_bf16_f32 v135, v76, v77
	v_add_u32_e32 v131, 0xa000, v130
	global_store_dwordx4 v131, v[132:135], s[36:37]
	s_nop 1
	v_cvt_pk_bf16_f32 v132, v86, v87
	v_cvt_pk_bf16_f32 v133, v88, v89
	v_cvt_pk_bf16_f32 v134, v78, v79
	v_cvt_pk_bf16_f32 v135, v80, v81
	v_add_u32_e32 v131, 0xc000, v130
	global_store_dwordx4 v131, v[132:135], s[36:37]
	s_nop 1
	v_cvt_pk_bf16_f32 v132, v70, v71
	v_cvt_pk_bf16_f32 v133, v72, v73
	v_cvt_pk_bf16_f32 v134, v66, v67
	v_cvt_pk_bf16_f32 v135, v68, v69
	v_add_u32_e32 v131, 0xe000, v130
	global_store_dwordx4 v131, v[132:135], s[36:37]
	s_nop 1
	v_cvt_pk_bf16_f32 v132, v62, v63
	v_cvt_pk_bf16_f32 v133, v64, v65
	v_cvt_pk_bf16_f32 v134, v58, v59
	v_cvt_pk_bf16_f32 v135, v60, v61
	v_add_u32_e32 v131, 0x10000, v130
	global_store_dwordx4 v131, v[132:135], s[36:37]
	s_nop 1
	v_cvt_pk_bf16_f32 v132, v50, v51
	v_cvt_pk_bf16_f32 v133, v52, v53
	v_cvt_pk_bf16_f32 v134, v42, v43
	v_cvt_pk_bf16_f32 v135, v44, v45
	v_add_u32_e32 v131, 0x12000, v130
	global_store_dwordx4 v131, v[132:135], s[36:37]
	s_nop 1
	v_cvt_pk_bf16_f32 v132, v54, v55
	v_cvt_pk_bf16_f32 v133, v56, v57
	v_cvt_pk_bf16_f32 v134, v46, v47
	v_cvt_pk_bf16_f32 v135, v48, v49
	v_add_u32_e32 v131, 0x14000, v130
	global_store_dwordx4 v131, v[132:135], s[36:37]
	s_nop 1
	v_cvt_pk_bf16_f32 v132, v34, v35
	v_cvt_pk_bf16_f32 v133, v36, v37
	v_cvt_pk_bf16_f32 v134, v26, v27
	v_cvt_pk_bf16_f32 v135, v28, v29
	v_add_u32_e32 v131, 0x16000, v130
	global_store_dwordx4 v131, v[132:135], s[36:37]
	s_nop 1
	v_cvt_pk_bf16_f32 v132, v38, v39
	v_cvt_pk_bf16_f32 v133, v40, v41
	v_cvt_pk_bf16_f32 v134, v30, v31
	v_cvt_pk_bf16_f32 v135, v32, v33
	v_add_u32_e32 v131, 0x18000, v130
	global_store_dwordx4 v131, v[132:135], s[36:37]
	s_nop 1
	v_cvt_pk_bf16_f32 v132, v18, v19
	v_cvt_pk_bf16_f32 v133, v20, v21
	v_cvt_pk_bf16_f32 v134, v10, v11
	v_cvt_pk_bf16_f32 v135, v12, v13
	v_add_u32_e32 v131, 0x1a000, v130
	global_store_dwordx4 v131, v[132:135], s[36:37]
	s_nop 1
	v_cvt_pk_bf16_f32 v132, v22, v23
	v_cvt_pk_bf16_f32 v133, v24, v25
	v_cvt_pk_bf16_f32 v134, v14, v15
	v_cvt_pk_bf16_f32 v135, v16, v17
	v_add_u32_e32 v131, 0x1c000, v130
	global_store_dwordx4 v131, v[132:135], s[36:37]
	s_nop 1
	v_cvt_pk_bf16_f32 v132, v6, v7
	v_cvt_pk_bf16_f32 v133, v8, v9
	v_cvt_pk_bf16_f32 v134, v2, v3
	v_cvt_pk_bf16_f32 v135, v4, v5
	v_add_u32_e32 v131, 0x1e000, v130
	global_store_dwordx4 v131, v[132:135], s[36:37]

; __device__ __forceinline__ void unpack8(const v4u w, float (&o)[8]) { o[0] = bflo(w.x); o[1] = bfhi(w.x); o[2] = bflo(w.y); o[3] = bfhi(w.y); o[4] = bflo(w.z); o[5] = bfhi(w.z); o[6] = bflo(w.w); o[7] = bfhi(w.w); }
; __device__ __forceinline__ v4u pack8(const float (&o)[8]) { v4u w; w.x = pk2(o[0], o[1]); w.y = pk2(o[2], o[3]); w.z = pk2(o[4], o[5]); w.w = pk2(o[6], o[7]); return w; }
; __device__ __forceinline__ float sigmf(float x) { return __builtin_amdgcn_rcpf(1.f + __expf(-x)); }
;     __device__ __forceinline__ void operator()(const f32x4 (&acc)[2][2][4][2], const pg8::Unit& u, int wr, int wc, int fr, int fq_in) const {
;         int fq = fq_in; asm volatile("" : "+v"(fq));
;         const int row0 = u.pm * 256 + wr * 64 + fr, col0 = u.pn * 256 + wc * 32 + 8 * fq; const bool first = u.sel == 0; const int goff = first ? 0 : D;
; #pragma unroll
;         for (int bj = 0; bj < 2; ++bj) {
;             const int col = col0 + bj * 128;
;             float b0[8];
;             { const f32x4 t0 = *(const f32x4*)(bg + goff + col), t1 = *(const f32x4*)(bg + goff + col + 4);
; #pragma unroll
;               for (int q = 0; q < 4; ++q) { b0[q] = t0[q]; b0[4 + q] = t1[q]; } }
; #pragma unroll
;             for (int ai = 0; ai < 2; ++ai) {
;                 v4u gw_[4], pw_[4];
; #pragma unroll
;                 for (int m = 0; m < 4; ++m) { const size_t row = (size_t)(row0 + ai * 128 + m * 16);
;                     gw_[m] = *(const v4u*)(Gt + row * (2 * D) + goff + col); pw_[m] = first ? (v4u){0u, 0u, 0u, 0u} : *(const v4u*)(O + row * D + col); }
;                 __builtin_amdgcn_sched_barrier(0);
; #pragma unroll
;                 for (int m = 0; m < 4; ++m) { const size_t row = (size_t)(row0 + ai * 128 + m * 16);
;                     float g0[8], p[8]; unpack8(gw_[m], g0); unpack8(pw_[m], p);
;                     float o[8];
; #pragma unroll
;                     for (int q = 0; q < 4; ++q) { o[q] = p[q] + sigmf(g0[q] + b0[q]) * acc[ai][bj][m][0][q]; o[4 + q] = p[4 + q] + sigmf(g0[4 + q] + b0[4 + q]) * acc[ai][bj][m][1][q]; }
;                     *(v4u*)(O + row * D + col) = pack8(o); }
.LBB0_903:
	s_lshl_b32 s98, s28, 4
	s_add_i32 s98, s98, s26
	s_cmp_lg_u64 s[30:31], 0
	s_cselect_b32 s99, 8, 0
	s_add_i32 s98, s98, s99
	s_lshl_b32 s98, s98, 17
	s_add_u32 s98, s48, s98
	s_addc_u32 s99, s49, 0
	s_lshl_b32 s8, s28, 20
	s_lshl_b32 s9, s26, 9
	s_add_i32 s8, s8, s9
	s_lshl_b32 s9, s50, 1
	s_add_i32 s8, s8, s9
	v_lshlrev_b32_e32 v226, 12, v216
	v_lshl_add_u32 v226, v1, 4, v226
	v_add_u32_e32 v226, s8, v226
	s_cmp_lg_u64 s[30:31], 0
	s_cselect_b32 s9, 0x2000, 0
	s_lshl_b32 s17, s26, 10
	s_add_i32 s9, s9, s17
	s_lshl_b32 s17, s50, 2
	s_add_i32 s9, s9, s17
	v_lshlrev_b32_e32 v252, 5, v1
	v_add_u32_e32 v252, s9, v252
	v_lshlrev_b32_e32 v227, 4, v0
	s_cmp_lg_u64 s[30:31], 0
	s_cbranch_scc1 .Lepi6_second
	global_load_dwordx4 v[244:247], v252, s[0:1]
	global_load_dwordx4 v[248:251], v252, s[0:1] offset:16
	global_load_dwordx4 v[114:117], v227, s[98:99]
	v_add_u32_e32 v254, 0x4000, v227
	global_load_dwordx4 v[118:121], v254, s[98:99]
	v_add_u32_e32 v254, 0x8000, v227
	global_load_dwordx4 v[138:141], v254, s[98:99]
	v_add_u32_e32 v254, 0xc000, v227
	global_load_dwordx4 v[142:145], v254, s[98:99]
	v_add_u32_e32 v254, 0x10000, v227
	global_load_dwordx4 v[146:149], v254, s[98:99]
	v_add_u32_e32 v254, 0x14000, v227
	global_load_dwordx4 v[150:153], v254, s[98:99]
	v_add_u32_e32 v254, 0x18000, v227
	global_load_dwordx4 v[154:157], v254, s[98:99]
	v_add_u32_e32 v254, 0x1c000, v227
	global_load_dwordx4 v[158:161], v254, s[98:99]
	v_add_u32_e32 v254, 0x2000, v227
	global_load_dwordx4 v[162:165], v254, s[98:99]
	v_add_u32_e32 v254, 0x6000, v227
	global_load_dwordx4 v[166:169], v254, s[98:99]
	v_add_u32_e32 v254, 0xa000, v227
	global_load_dwordx4 v[190:193], v254, s[98:99]
	v_add_u32_e32 v254, 0xe000, v227
	global_load_dwordx4 v[194:197], v254, s[98:99]
	v_add_u32_e32 v254, 0x12000, v227
	global_load_dwordx4 v[198:201], v254, s[98:99]
	v_add_u32_e32 v254, 0x16000, v227
	global_load_dwordx4 v[202:205], v254, s[98:99]
	v_add_u32_e32 v254, 0x1a000, v227
	global_load_dwordx4 v[206:209], v254, s[98:99]
	v_add_u32_e32 v254, 0x1e000, v227
	global_load_dwordx4 v[210:213], v254, s[98:99]
	v_mov_b32_e32 v228, 0
	v_mov_b32_e32 v229, 0
	v_mov_b32_e32 v230, 0
	v_mov_b32_e32 v231, 0
	v_mov_b32_e32 v232, 0
	v_mov_b32_e32 v233, 0
	v_mov_b32_e32 v234, 0
	v_mov_b32_e32 v235, 0
	v_mov_b32_e32 v236, 0
	v_mov_b32_e32 v237, 0
	v_mov_b32_e32 v238, 0
	v_mov_b32_e32 v239, 0
	v_mov_b32_e32 v240, 0
	v_mov_b32_e32 v241, 0
	v_mov_b32_e32 v242, 0
	v_mov_b32_e32 v243, 0
	s_waitcnt vmcnt(16)
	s_waitcnt vmcnt(15)
	v_lshlrev_b32_e32 v170, 16, v114
	v_and_b32_e32 v114, 0xffff0000, v114
	v_lshlrev_b32_e32 v171, 16, v115
	v_and_b32_e32 v115, 0xffff0000, v115
	v_lshlrev_b32_e32 v214, 16, v116
	v_and_b32_e32 v116, 0xffff0000, v116
	v_lshlrev_b32_e32 v215, 16, v117
	v_and_b32_e32 v117, 0xffff0000, v117
	v_add_f32_e32 v170, v244, v170
	v_add_f32_e32 v114, v245, v114
	v_add_f32_e32 v171, v246, v171
	v_add_f32_e32 v115, v247, v115
	v_add_f32_e32 v214, v248, v214
	v_add_f32_e32 v116, v249, v116
	v_add_f32_e32 v215, v250, v215
	v_add_f32_e32 v117, v251, v117
	v_mul_f32_e32 v170, 0xbfb8aa3b, v170
	v_mul_f32_e32 v114, 0xbfb8aa3b, v114
	v_mul_f32_e32 v171, 0xbfb8aa3b, v171
	v_mul_f32_e32 v115, 0xbfb8aa3b, v115
	v_mul_f32_e32 v214, 0xbfb8aa3b, v214
	v_mul_f32_e32 v116, 0xbfb8aa3b, v116
	v_mul_f32_e32 v215, 0xbfb8aa3b, v215
	v_mul_f32_e32 v117, 0xbfb8aa3b, v117
	v_exp_f32_e32 v170, v170
	v_exp_f32_e32 v114, v114
	v_exp_f32_e32 v171, v171
	v_exp_f32_e32 v115, v115
	v_exp_f32_e32 v214, v214
	v_exp_f32_e32 v116, v116
	v_exp_f32_e32 v215, v215
	v_exp_f32_e32 v117, v117
	v_add_f32_e32 v170, 1.0, v170
	v_add_f32_e32 v114, 1.0, v114
	v_add_f32_e32 v171, 1.0, v171
	v_add_f32_e32 v115, 1.0, v115
	v_add_f32_e32 v214, 1.0, v214
	v_add_f32_e32 v116, 1.0, v116
	v_add_f32_e32 v215, 1.0, v215
	v_add_f32_e32 v117, 1.0, v117
	v_rcp_f32_e32 v170, v170
	v_rcp_f32_e32 v114, v114
	v_rcp_f32_e32 v171, v171
	v_rcp_f32_e32 v115, v115
	v_rcp_f32_e32 v214, v214
	v_rcp_f32_e32 v116, v116
	v_rcp_f32_e32 v215, v215
	v_rcp_f32_e32 v117, v117
	v_fma_f32 v134, v134, v170, v228
	v_fma_f32 v135, v135, v114, v228
	v_fma_f32 v136, v136, v171, v228
	v_fma_f32 v137, v137, v115, v228
	v_fma_f32 v130, v130, v214, v228
	v_fma_f32 v131, v131, v116, v228
	v_fma_f32 v132, v132, v215, v228
	v_fma_f32 v133, v133, v117, v228
	v_cvt_pk_bf16_f32 v134, v134, v135
	v_cvt_pk_bf16_f32 v135, v136, v137
	v_cvt_pk_bf16_f32 v136, v130, v131
	v_cvt_pk_bf16_f32 v137, v132, v133
	global_store_dwordx4 v226, v[134:137], s[4:5]
	s_waitcnt vmcnt(15)
	v_lshlrev_b32_e32 v170, 16, v118
	v_and_b32_e32 v118, 0xffff0000, v118
	v_lshlrev_b32_e32 v171, 16, v119
	v_and_b32_e32 v119, 0xffff0000, v119
	v_lshlrev_b32_e32 v214, 16, v120
	v_and_b32_e32 v120, 0xffff0000, v120
	v_lshlrev_b32_e32 v215, 16, v121
	v_and_b32_e32 v121, 0xffff0000, v121
	v_add_f32_e32 v170, v244, v170
	v_add_f32_e32 v118, v245, v118
	v_add_f32_e32 v171, v246, v171
	v_add_f32_e32 v119, v247, v119
	v_add_f32_e32 v214, v248, v214
	v_add_f32_e32 v120, v249, v120
	v_add_f32_e32 v215, v250, v215
	v_add_f32_e32 v121, v251, v121
	v_mul_f32_e32 v170, 0xbfb8aa3b, v170
	v_mul_f32_e32 v118, 0xbfb8aa3b, v118
	v_mul_f32_e32 v171, 0xbfb8aa3b, v171
	v_mul_f32_e32 v119, 0xbfb8aa3b, v119
	v_mul_f32_e32 v214, 0xbfb8aa3b, v214
	v_mul_f32_e32 v120, 0xbfb8aa3b, v120
	v_mul_f32_e32 v215, 0xbfb8aa3b, v215
	v_mul_f32_e32 v121, 0xbfb8aa3b, v121
	v_exp_f32_e32 v170, v170
	v_exp_f32_e32 v118, v118
	v_exp_f32_e32 v171, v171
	v_exp_f32_e32 v119, v119
	v_exp_f32_e32 v214, v214
	v_exp_f32_e32 v120, v120
	v_exp_f32_e32 v215, v215
	v_exp_f32_e32 v121, v121
	v_add_f32_e32 v170, 1.0, v170
	v_add_f32_e32 v118, 1.0, v118
	v_add_f32_e32 v171, 1.0, v171
	v_add_f32_e32 v119, 1.0, v119
	v_add_f32_e32 v214, 1.0, v214
	v_add_f32_e32 v120, 1.0, v120
	v_add_f32_e32 v215, 1.0, v215
	v_add_f32_e32 v121, 1.0, v121
	v_rcp_f32_e32 v170, v170
	v_rcp_f32_e32 v118, v118
	v_rcp_f32_e32 v171, v171
	v_rcp_f32_e32 v119, v119
	v_rcp_f32_e32 v214, v214
	v_rcp_f32_e32 v120, v120
	v_rcp_f32_e32 v215, v215
	v_rcp_f32_e32 v121, v121
	v_fma_f32 v126, v126, v170, v232
	v_fma_f32 v127, v127, v118, v232
	v_fma_f32 v128, v128, v171, v232
	v_fma_f32 v129, v129, v119, v232
	v_fma_f32 v122, v122, v214, v232
	v_fma_f32 v123, v123, v120, v232
	v_fma_f32 v124, v124, v215, v232
	v_fma_f32 v125, v125, v121, v232
	v_cvt_pk_bf16_f32 v126, v126, v127
	v_cvt_pk_bf16_f32 v127, v128, v129
	v_cvt_pk_bf16_f32 v128, v122, v123
	v_cvt_pk_bf16_f32 v129, v124, v125
	v_add_u32_e32 v225, 0x10000, v226
	global_store_dwordx4 v225, v[126:129], s[4:5]
	global_load_dwordx4 v[130:133], v252, s[0:1] offset:512
	global_load_dwordx4 v[122:125], v252, s[0:1] offset:528
	s_waitcnt vmcnt(17)
; __device__ __forceinline__ void unpack8(const v4u w, float (&o)[8]) { o[0] = bflo(w.x); o[1] = bfhi(w.x); o[2] = bflo(w.y); o[3] = bfhi(w.y); o[4] = bflo(w.z); o[5] = bfhi(w.z); o[6] = bflo(w.w); o[7] = bfhi(w.w); }
; __device__ __forceinline__ v4u pack8(const float (&o)[8]) { v4u w; w.x = pk2(o[0], o[1]); w.y = pk2(o[2], o[3]); w.z = pk2(o[4], o[5]); w.w = pk2(o[6], o[7]); return w; }
; __device__ __forceinline__ float sigmf(float x) { return __builtin_amdgcn_rcpf(1.f + __expf(-x)); }
;     __device__ __forceinline__ void operator()(const f32x4 (&acc)[2][2][4][2], const pg8::Unit& u, int wr, int wc, int fr, int fq_in) const {
;     ...
;                 for (int m = 0; m < 4; ++m) { const size_t row = (size_t)(row0 + ai * 128 + m * 16);
;                     gw_[m] = *(const v4u*)(Gt + row * (2 * D) + goff + col); pw_[m] = first ? (v4u){0u, 0u, 0u, 0u} : *(const v4u*)(O + row * D + col); }
;                 __builtin_amdgcn_sched_barrier(0);
; #pragma unroll
;                 for (int m = 0; m < 4; ++m) { const size_t row = (size_t)(row0 + ai * 128 + m * 16);
;                     float g0[8], p[8]; unpack8(gw_[m], g0); unpack8(pw_[m], p);
;                     float o[8];
; #pragma unroll
;                     for (int q = 0; q < 4; ++q) { o[q] = p[q] + sigmf(g0[q] + b0[q]) * acc[ai][bj][m][0][q]; o[4 + q] = p[4 + q] + sigmf(g0[4 + q] + b0[4 + q]) * acc[ai][bj][m][1][q]; }
;                     *(v4u*)(O + row * D + col) = pack8(o); }
	v_lshlrev_b32_e32 v170, 16, v138
	v_and_b32_e32 v138, 0xffff0000, v138
	v_lshlrev_b32_e32 v171, 16, v139
	v_and_b32_e32 v139, 0xffff0000, v139
	v_lshlrev_b32_e32 v214, 16, v140
	v_and_b32_e32 v140, 0xffff0000, v140
	v_lshlrev_b32_e32 v215, 16, v141
	v_and_b32_e32 v141, 0xffff0000, v141
	v_add_f32_e32 v170, v244, v170
	v_add_f32_e32 v138, v245, v138
	v_add_f32_e32 v171, v246, v171
	v_add_f32_e32 v139, v247, v139
	v_add_f32_e32 v214, v248, v214
	v_add_f32_e32 v140, v249, v140
	v_add_f32_e32 v215, v250, v215
	v_add_f32_e32 v141, v251, v141
	v_mul_f32_e32 v170, 0xbfb8aa3b, v170
	v_mul_f32_e32 v138, 0xbfb8aa3b, v138
	v_mul_f32_e32 v171, 0xbfb8aa3b, v171
	v_mul_f32_e32 v139, 0xbfb8aa3b, v139
	v_mul_f32_e32 v214, 0xbfb8aa3b, v214
	v_mul_f32_e32 v140, 0xbfb8aa3b, v140
	v_mul_f32_e32 v215, 0xbfb8aa3b, v215
	v_mul_f32_e32 v141, 0xbfb8aa3b, v141
	v_exp_f32_e32 v170, v170
	v_exp_f32_e32 v138, v138
	v_exp_f32_e32 v171, v171
	v_exp_f32_e32 v139, v139
	v_exp_f32_e32 v214, v214
	v_exp_f32_e32 v140, v140
	v_exp_f32_e32 v215, v215
	v_exp_f32_e32 v141, v141
	v_add_f32_e32 v170, 1.0, v170
	v_add_f32_e32 v138, 1.0, v138
	v_add_f32_e32 v171, 1.0, v171
	v_add_f32_e32 v139, 1.0, v139
	v_add_f32_e32 v214, 1.0, v214
	v_add_f32_e32 v140, 1.0, v140
	v_add_f32_e32 v215, 1.0, v215
	v_add_f32_e32 v141, 1.0, v141
	v_rcp_f32_e32 v170, v170
	v_rcp_f32_e32 v138, v138
	v_rcp_f32_e32 v171, v171
	v_rcp_f32_e32 v139, v139
	v_rcp_f32_e32 v214, v214
	v_rcp_f32_e32 v140, v140
	v_rcp_f32_e32 v215, v215
	v_rcp_f32_e32 v141, v141
	v_fma_f32 v110, v110, v170, v236
	v_fma_f32 v111, v111, v138, v236
	v_fma_f32 v112, v112, v171, v236
	v_fma_f32 v113, v113, v139, v236
	v_fma_f32 v106, v106, v214, v236
	v_fma_f32 v107, v107, v140, v236
	v_fma_f32 v108, v108, v215, v236
	v_fma_f32 v109, v109, v141, v236
	v_cvt_pk_bf16_f32 v110, v110, v111
	v_cvt_pk_bf16_f32 v111, v112, v113
	v_cvt_pk_bf16_f32 v112, v106, v107
	v_cvt_pk_bf16_f32 v113, v108, v109
	v_add_u32_e32 v225, 0x20000, v226
	global_store_dwordx4 v225, v[110:113], s[4:5]
	s_waitcnt vmcnt(17)
	v_lshlrev_b32_e32 v170, 16, v142
	v_and_b32_e32 v142, 0xffff0000, v142
	v_lshlrev_b32_e32 v171, 16, v143
	v_and_b32_e32 v143, 0xffff0000, v143
	v_lshlrev_b32_e32 v214, 16, v144
	v_and_b32_e32 v144, 0xffff0000, v144
	v_lshlrev_b32_e32 v215, 16, v145
	v_and_b32_e32 v145, 0xffff0000, v145
	v_add_f32_e32 v170, v244, v170
	v_add_f32_e32 v142, v245, v142
	v_add_f32_e32 v171, v246, v171
	v_add_f32_e32 v143, v247, v143
	v_add_f32_e32 v214, v248, v214
	v_add_f32_e32 v144, v249, v144
	v_add_f32_e32 v215, v250, v215
	v_add_f32_e32 v145, v251, v145
	v_mul_f32_e32 v170, 0xbfb8aa3b, v170
	v_mul_f32_e32 v142, 0xbfb8aa3b, v142
	v_mul_f32_e32 v171, 0xbfb8aa3b, v171
	v_mul_f32_e32 v143, 0xbfb8aa3b, v143
	v_mul_f32_e32 v214, 0xbfb8aa3b, v214
	v_mul_f32_e32 v144, 0xbfb8aa3b, v144
	v_mul_f32_e32 v215, 0xbfb8aa3b, v215
	v_mul_f32_e32 v145, 0xbfb8aa3b, v145
	v_exp_f32_e32 v170, v170
	v_exp_f32_e32 v142, v142
	v_exp_f32_e32 v171, v171
	v_exp_f32_e32 v143, v143
	v_exp_f32_e32 v214, v214
	v_exp_f32_e32 v144, v144
	v_exp_f32_e32 v215, v215
	v_exp_f32_e32 v145, v145
	v_add_f32_e32 v170, 1.0, v170
	v_add_f32_e32 v142, 1.0, v142
	v_add_f32_e32 v171, 1.0, v171
	v_add_f32_e32 v143, 1.0, v143
	v_add_f32_e32 v214, 1.0, v214
	v_add_f32_e32 v144, 1.0, v144
	v_add_f32_e32 v215, 1.0, v215
	v_add_f32_e32 v145, 1.0, v145
	v_rcp_f32_e32 v170, v170
	v_rcp_f32_e32 v142, v142
	v_rcp_f32_e32 v171, v171
	v_rcp_f32_e32 v143, v143
	v_rcp_f32_e32 v214, v214
	v_rcp_f32_e32 v144, v144
	v_rcp_f32_e32 v215, v215
	v_rcp_f32_e32 v145, v145
	v_fma_f32 v102, v102, v170, v240
	v_fma_f32 v103, v103, v142, v240
	v_fma_f32 v104, v104, v171, v240
	v_fma_f32 v105, v105, v143, v240
	v_fma_f32 v98, v98, v214, v240
	v_fma_f32 v99, v99, v144, v240
	v_fma_f32 v100, v100, v215, v240
	v_fma_f32 v101, v101, v145, v240
	v_cvt_pk_bf16_f32 v102, v102, v103
	v_cvt_pk_bf16_f32 v103, v104, v105
	v_cvt_pk_bf16_f32 v104, v98, v99
	v_cvt_pk_bf16_f32 v105, v100, v101
	v_add_u32_e32 v225, 0x30000, v226
	global_store_dwordx4 v225, v[102:105], s[4:5]
	s_waitcnt vmcnt(17)
	v_lshlrev_b32_e32 v170, 16, v146
	v_and_b32_e32 v146, 0xffff0000, v146
	v_lshlrev_b32_e32 v171, 16, v147
	v_and_b32_e32 v147, 0xffff0000, v147
	v_lshlrev_b32_e32 v214, 16, v148
	v_and_b32_e32 v148, 0xffff0000, v148
	v_lshlrev_b32_e32 v215, 16, v149
	v_and_b32_e32 v149, 0xffff0000, v149
	v_add_f32_e32 v170, v244, v170
	v_add_f32_e32 v146, v245, v146
	v_add_f32_e32 v171, v246, v171
	v_add_f32_e32 v147, v247, v147
	v_add_f32_e32 v214, v248, v214
	v_add_f32_e32 v148, v249, v148
	v_add_f32_e32 v215, v250, v215
	v_add_f32_e32 v149, v251, v149
	v_mul_f32_e32 v170, 0xbfb8aa3b, v170
	v_mul_f32_e32 v146, 0xbfb8aa3b, v146
	v_mul_f32_e32 v171, 0xbfb8aa3b, v171
	v_mul_f32_e32 v147, 0xbfb8aa3b, v147
	v_mul_f32_e32 v214, 0xbfb8aa3b, v214
	v_mul_f32_e32 v148, 0xbfb8aa3b, v148
	v_mul_f32_e32 v215, 0xbfb8aa3b, v215
	v_mul_f32_e32 v149, 0xbfb8aa3b, v149
	v_exp_f32_e32 v170, v170
	v_exp_f32_e32 v146, v146
	v_exp_f32_e32 v171, v171
	v_exp_f32_e32 v147, v147
	v_exp_f32_e32 v214, v214
	v_exp_f32_e32 v148, v148
	v_exp_f32_e32 v215, v215
	v_exp_f32_e32 v149, v149
	v_add_f32_e32 v170, 1.0, v170
	v_add_f32_e32 v146, 1.0, v146
	v_add_f32_e32 v171, 1.0, v171
	v_add_f32_e32 v147, 1.0, v147
	v_add_f32_e32 v214, 1.0, v214
	v_add_f32_e32 v148, 1.0, v148
	v_add_f32_e32 v215, 1.0, v215
	v_add_f32_e32 v149, 1.0, v149
	v_rcp_f32_e32 v170, v170
	v_rcp_f32_e32 v146, v146
	v_rcp_f32_e32 v171, v171
	v_rcp_f32_e32 v147, v147
	v_rcp_f32_e32 v214, v214
	v_rcp_f32_e32 v148, v148
	v_rcp_f32_e32 v215, v215
	v_rcp_f32_e32 v149, v149
	v_fma_f32 v94, v94, v170, v228
	v_fma_f32 v95, v95, v146, v228
	v_fma_f32 v96, v96, v171, v228
	v_fma_f32 v97, v97, v147, v228
	v_fma_f32 v90, v90, v214, v228
	v_fma_f32 v91, v91, v148, v228
	v_fma_f32 v92, v92, v215, v228
	v_fma_f32 v93, v93, v149, v228
	v_cvt_pk_bf16_f32 v94, v94, v95
	v_cvt_pk_bf16_f32 v95, v96, v97
	v_cvt_pk_bf16_f32 v96, v90, v91
	v_cvt_pk_bf16_f32 v97, v92, v93
	v_add_u32_e32 v225, 0x80000, v226
	global_store_dwordx4 v225, v[94:97], s[4:5]
	s_waitcnt vmcnt(17)
; __device__ __forceinline__ void unpack8(const v4u w, float (&o)[8]) { o[0] = bflo(w.x); o[1] = bfhi(w.x); o[2] = bflo(w.y); o[3] = bfhi(w.y); o[4] = bflo(w.z); o[5] = bfhi(w.z); o[6] = bflo(w.w); o[7] = bfhi(w.w); }
; __device__ __forceinline__ v4u pack8(const float (&o)[8]) { v4u w; w.x = pk2(o[0], o[1]); w.y = pk2(o[2], o[3]); w.z = pk2(o[4], o[5]); w.w = pk2(o[6], o[7]); return w; }
; __device__ __forceinline__ float sigmf(float x) { return __builtin_amdgcn_rcpf(1.f + __expf(-x)); }
;     __device__ __forceinline__ void operator()(const f32x4 (&acc)[2][2][4][2], const pg8::Unit& u, int wr, int wc, int fr, int fq_in) const {
;     ...
;                 for (int m = 0; m < 4; ++m) { const size_t row = (size_t)(row0 + ai * 128 + m * 16);
;                     gw_[m] = *(const v4u*)(Gt + row * (2 * D) + goff + col); pw_[m] = first ? (v4u){0u, 0u, 0u, 0u} : *(const v4u*)(O + row * D + col); }
;                 __builtin_amdgcn_sched_barrier(0);
; #pragma unroll
;                 for (int m = 0; m < 4; ++m) { const size_t row = (size_t)(row0 + ai * 128 + m * 16);
;                     float g0[8], p[8]; unpack8(gw_[m], g0); unpack8(pw_[m], p);
;                     float o[8];
; #pragma unroll
;                     for (int q = 0; q < 4; ++q) { o[q] = p[q] + sigmf(g0[q] + b0[q]) * acc[ai][bj][m][0][q]; o[4 + q] = p[4 + q] + sigmf(g0[4 + q] + b0[4 + q]) * acc[ai][bj][m][1][q]; }
;                     *(v4u*)(O + row * D + col) = pack8(o); }
	v_lshlrev_b32_e32 v170, 16, v150
	v_and_b32_e32 v150, 0xffff0000, v150
	v_lshlrev_b32_e32 v171, 16, v151
	v_and_b32_e32 v151, 0xffff0000, v151
	v_lshlrev_b32_e32 v214, 16, v152
	v_and_b32_e32 v152, 0xffff0000, v152
	v_lshlrev_b32_e32 v215, 16, v153
	v_and_b32_e32 v153, 0xffff0000, v153
	v_add_f32_e32 v170, v244, v170
	v_add_f32_e32 v150, v245, v150
	v_add_f32_e32 v171, v246, v171
	v_add_f32_e32 v151, v247, v151
	v_add_f32_e32 v214, v248, v214
	v_add_f32_e32 v152, v249, v152
	v_add_f32_e32 v215, v250, v215
	v_add_f32_e32 v153, v251, v153
	v_mul_f32_e32 v170, 0xbfb8aa3b, v170
	v_mul_f32_e32 v150, 0xbfb8aa3b, v150
	v_mul_f32_e32 v171, 0xbfb8aa3b, v171
	v_mul_f32_e32 v151, 0xbfb8aa3b, v151
	v_mul_f32_e32 v214, 0xbfb8aa3b, v214
	v_mul_f32_e32 v152, 0xbfb8aa3b, v152
	v_mul_f32_e32 v215, 0xbfb8aa3b, v215
	v_mul_f32_e32 v153, 0xbfb8aa3b, v153
	v_exp_f32_e32 v170, v170
	v_exp_f32_e32 v150, v150
	v_exp_f32_e32 v171, v171
	v_exp_f32_e32 v151, v151
	v_exp_f32_e32 v214, v214
	v_exp_f32_e32 v152, v152
	v_exp_f32_e32 v215, v215
	v_exp_f32_e32 v153, v153
	v_add_f32_e32 v170, 1.0, v170
	v_add_f32_e32 v150, 1.0, v150
	v_add_f32_e32 v171, 1.0, v171
	v_add_f32_e32 v151, 1.0, v151
	v_add_f32_e32 v214, 1.0, v214
	v_add_f32_e32 v152, 1.0, v152
	v_add_f32_e32 v215, 1.0, v215
	v_add_f32_e32 v153, 1.0, v153
	v_rcp_f32_e32 v170, v170
	v_rcp_f32_e32 v150, v150
	v_rcp_f32_e32 v171, v171
	v_rcp_f32_e32 v151, v151
	v_rcp_f32_e32 v214, v214
	v_rcp_f32_e32 v152, v152
	v_rcp_f32_e32 v215, v215
	v_rcp_f32_e32 v153, v153
	v_fma_f32 v86, v86, v170, v232
	v_fma_f32 v87, v87, v150, v232
	v_fma_f32 v88, v88, v171, v232
	v_fma_f32 v89, v89, v151, v232
	v_fma_f32 v82, v82, v214, v232
	v_fma_f32 v83, v83, v152, v232
	v_fma_f32 v84, v84, v215, v232
	v_fma_f32 v85, v85, v153, v232
	v_cvt_pk_bf16_f32 v86, v86, v87
	v_cvt_pk_bf16_f32 v87, v88, v89
	v_cvt_pk_bf16_f32 v88, v82, v83
	v_cvt_pk_bf16_f32 v89, v84, v85
	v_add_u32_e32 v225, 0x90000, v226
	global_store_dwordx4 v225, v[86:89], s[4:5]
	s_waitcnt vmcnt(17)
	v_lshlrev_b32_e32 v170, 16, v154
	v_and_b32_e32 v154, 0xffff0000, v154
	v_lshlrev_b32_e32 v171, 16, v155
	v_and_b32_e32 v155, 0xffff0000, v155
	v_lshlrev_b32_e32 v214, 16, v156
	v_and_b32_e32 v156, 0xffff0000, v156
	v_lshlrev_b32_e32 v215, 16, v157
	v_and_b32_e32 v157, 0xffff0000, v157
	v_add_f32_e32 v170, v244, v170
	v_add_f32_e32 v154, v245, v154
	v_add_f32_e32 v171, v246, v171
	v_add_f32_e32 v155, v247, v155
	v_add_f32_e32 v214, v248, v214
	v_add_f32_e32 v156, v249, v156
	v_add_f32_e32 v215, v250, v215
	v_add_f32_e32 v157, v251, v157
	v_mul_f32_e32 v170, 0xbfb8aa3b, v170
	v_mul_f32_e32 v154, 0xbfb8aa3b, v154
	v_mul_f32_e32 v171, 0xbfb8aa3b, v171
	v_mul_f32_e32 v155, 0xbfb8aa3b, v155
	v_mul_f32_e32 v214, 0xbfb8aa3b, v214
	v_mul_f32_e32 v156, 0xbfb8aa3b, v156
	v_mul_f32_e32 v215, 0xbfb8aa3b, v215
	v_mul_f32_e32 v157, 0xbfb8aa3b, v157
	v_exp_f32_e32 v170, v170
	v_exp_f32_e32 v154, v154
	v_exp_f32_e32 v171, v171
	v_exp_f32_e32 v155, v155
	v_exp_f32_e32 v214, v214
	v_exp_f32_e32 v156, v156
	v_exp_f32_e32 v215, v215
	v_exp_f32_e32 v157, v157
	v_add_f32_e32 v170, 1.0, v170
	v_add_f32_e32 v154, 1.0, v154
	v_add_f32_e32 v171, 1.0, v171
	v_add_f32_e32 v155, 1.0, v155
	v_add_f32_e32 v214, 1.0, v214
	v_add_f32_e32 v156, 1.0, v156
	v_add_f32_e32 v215, 1.0, v215
	v_add_f32_e32 v157, 1.0, v157
	v_rcp_f32_e32 v170, v170
	v_rcp_f32_e32 v154, v154
	v_rcp_f32_e32 v171, v171
	v_rcp_f32_e32 v155, v155
	v_rcp_f32_e32 v214, v214
	v_rcp_f32_e32 v156, v156
	v_rcp_f32_e32 v215, v215
	v_rcp_f32_e32 v157, v157
	v_fma_f32 v78, v78, v170, v236
	v_fma_f32 v79, v79, v154, v236
	v_fma_f32 v80, v80, v171, v236
	v_fma_f32 v81, v81, v155, v236
	v_fma_f32 v74, v74, v214, v236
	v_fma_f32 v75, v75, v156, v236
	v_fma_f32 v76, v76, v215, v236
	v_fma_f32 v77, v77, v157, v236
	v_cvt_pk_bf16_f32 v78, v78, v79
	v_cvt_pk_bf16_f32 v79, v80, v81
	v_cvt_pk_bf16_f32 v80, v74, v75
	v_cvt_pk_bf16_f32 v81, v76, v77
	v_add_u32_e32 v225, 0xa0000, v226
	global_store_dwordx4 v225, v[78:81], s[4:5]
	s_waitcnt vmcnt(17)
	v_lshlrev_b32_e32 v170, 16, v158
	v_and_b32_e32 v158, 0xffff0000, v158
	v_lshlrev_b32_e32 v171, 16, v159
	v_and_b32_e32 v159, 0xffff0000, v159
	v_lshlrev_b32_e32 v214, 16, v160
	v_and_b32_e32 v160, 0xffff0000, v160
	v_lshlrev_b32_e32 v215, 16, v161
	v_and_b32_e32 v161, 0xffff0000, v161
	v_add_f32_e32 v170, v244, v170
	v_add_f32_e32 v158, v245, v158
	v_add_f32_e32 v171, v246, v171
	v_add_f32_e32 v159, v247, v159
	v_add_f32_e32 v214, v248, v214
	v_add_f32_e32 v160, v249, v160
	v_add_f32_e32 v215, v250, v215
	v_add_f32_e32 v161, v251, v161
	v_mul_f32_e32 v170, 0xbfb8aa3b, v170
	v_mul_f32_e32 v158, 0xbfb8aa3b, v158
	v_mul_f32_e32 v171, 0xbfb8aa3b, v171
	v_mul_f32_e32 v159, 0xbfb8aa3b, v159
	v_mul_f32_e32 v214, 0xbfb8aa3b, v214
	v_mul_f32_e32 v160, 0xbfb8aa3b, v160
	v_mul_f32_e32 v215, 0xbfb8aa3b, v215
	v_mul_f32_e32 v161, 0xbfb8aa3b, v161
	v_exp_f32_e32 v170, v170
	v_exp_f32_e32 v158, v158
	v_exp_f32_e32 v171, v171
	v_exp_f32_e32 v159, v159
	v_exp_f32_e32 v214, v214
	v_exp_f32_e32 v160, v160
	v_exp_f32_e32 v215, v215
	v_exp_f32_e32 v161, v161
	v_add_f32_e32 v170, 1.0, v170
	v_add_f32_e32 v158, 1.0, v158
	v_add_f32_e32 v171, 1.0, v171
	v_add_f32_e32 v159, 1.0, v159
	v_add_f32_e32 v214, 1.0, v214
	v_add_f32_e32 v160, 1.0, v160
	v_add_f32_e32 v215, 1.0, v215
	v_add_f32_e32 v161, 1.0, v161
	v_rcp_f32_e32 v170, v170
	v_rcp_f32_e32 v158, v158
	v_rcp_f32_e32 v171, v171
	v_rcp_f32_e32 v159, v159
	v_rcp_f32_e32 v214, v214
	v_rcp_f32_e32 v160, v160
	v_rcp_f32_e32 v215, v215
	v_rcp_f32_e32 v161, v161
	v_fma_f32 v70, v70, v170, v240
	v_fma_f32 v71, v71, v158, v240
	v_fma_f32 v72, v72, v171, v240
	v_fma_f32 v73, v73, v159, v240
	v_fma_f32 v66, v66, v214, v240
	v_fma_f32 v67, v67, v160, v240
	v_fma_f32 v68, v68, v215, v240
	v_fma_f32 v69, v69, v161, v240
	v_cvt_pk_bf16_f32 v70, v70, v71
	v_cvt_pk_bf16_f32 v71, v72, v73
	v_cvt_pk_bf16_f32 v72, v66, v67
	v_cvt_pk_bf16_f32 v73, v68, v69
	v_add_u32_e32 v225, 0xb0000, v226
	global_store_dwordx4 v225, v[70:73], s[4:5]
	s_waitcnt vmcnt(6)
; __device__ __forceinline__ void unpack8(const v4u w, float (&o)[8]) { o[0] = bflo(w.x); o[1] = bfhi(w.x); o[2] = bflo(w.y); o[3] = bfhi(w.y); o[4] = bflo(w.z); o[5] = bfhi(w.z); o[6] = bflo(w.w); o[7] = bfhi(w.w); }
; __device__ __forceinline__ v4u pack8(const float (&o)[8]) { v4u w; w.x = pk2(o[0], o[1]); w.y = pk2(o[2], o[3]); w.z = pk2(o[4], o[5]); w.w = pk2(o[6], o[7]); return w; }
; __device__ __forceinline__ float sigmf(float x) { return __builtin_amdgcn_rcpf(1.f + __expf(-x)); }
;     __device__ __forceinline__ void operator()(const f32x4 (&acc)[2][2][4][2], const pg8::Unit& u, int wr, int wc, int fr, int fq_in) const {
;     ...
;                 for (int m = 0; m < 4; ++m) { const size_t row = (size_t)(row0 + ai * 128 + m * 16);
;                     gw_[m] = *(const v4u*)(Gt + row * (2 * D) + goff + col); pw_[m] = first ? (v4u){0u, 0u, 0u, 0u} : *(const v4u*)(O + row * D + col); }
;                 __builtin_amdgcn_sched_barrier(0);
; #pragma unroll
;                 for (int m = 0; m < 4; ++m) { const size_t row = (size_t)(row0 + ai * 128 + m * 16);
;                     float g0[8], p[8]; unpack8(gw_[m], g0); unpack8(pw_[m], p);
;                     float o[8];
; #pragma unroll
;                     for (int q = 0; q < 4; ++q) { o[q] = p[q] + sigmf(g0[q] + b0[q]) * acc[ai][bj][m][0][q]; o[4 + q] = p[4 + q] + sigmf(g0[4 + q] + b0[4 + q]) * acc[ai][bj][m][1][q]; }
;                     *(v4u*)(O + row * D + col) = pack8(o); }
	s_waitcnt vmcnt(17)
	v_lshlrev_b32_e32 v170, 16, v162
	v_and_b32_e32 v162, 0xffff0000, v162
	v_lshlrev_b32_e32 v171, 16, v163
	v_and_b32_e32 v163, 0xffff0000, v163
	v_lshlrev_b32_e32 v214, 16, v164
	v_and_b32_e32 v164, 0xffff0000, v164
	v_lshlrev_b32_e32 v215, 16, v165
	v_and_b32_e32 v165, 0xffff0000, v165
	v_add_f32_e32 v170, v130, v170
	v_add_f32_e32 v162, v131, v162
	v_add_f32_e32 v171, v132, v171
	v_add_f32_e32 v163, v133, v163
	v_add_f32_e32 v214, v122, v214
	v_add_f32_e32 v164, v123, v164
	v_add_f32_e32 v215, v124, v215
	v_add_f32_e32 v165, v125, v165
	v_mul_f32_e32 v170, 0xbfb8aa3b, v170
	v_mul_f32_e32 v162, 0xbfb8aa3b, v162
	v_mul_f32_e32 v171, 0xbfb8aa3b, v171
	v_mul_f32_e32 v163, 0xbfb8aa3b, v163
	v_mul_f32_e32 v214, 0xbfb8aa3b, v214
	v_mul_f32_e32 v164, 0xbfb8aa3b, v164
	v_mul_f32_e32 v215, 0xbfb8aa3b, v215
	v_mul_f32_e32 v165, 0xbfb8aa3b, v165
	v_exp_f32_e32 v170, v170
	v_exp_f32_e32 v162, v162
	v_exp_f32_e32 v171, v171
	v_exp_f32_e32 v163, v163
	v_exp_f32_e32 v214, v214
	v_exp_f32_e32 v164, v164
	v_exp_f32_e32 v215, v215
	v_exp_f32_e32 v165, v165
	v_add_f32_e32 v170, 1.0, v170
	v_add_f32_e32 v162, 1.0, v162
	v_add_f32_e32 v171, 1.0, v171
	v_add_f32_e32 v163, 1.0, v163
	v_add_f32_e32 v214, 1.0, v214
	v_add_f32_e32 v164, 1.0, v164
	v_add_f32_e32 v215, 1.0, v215
	v_add_f32_e32 v165, 1.0, v165
	v_rcp_f32_e32 v170, v170
	v_rcp_f32_e32 v162, v162
	v_rcp_f32_e32 v171, v171
	v_rcp_f32_e32 v163, v163
	v_rcp_f32_e32 v214, v214
	v_rcp_f32_e32 v164, v164
	v_rcp_f32_e32 v215, v215
	v_rcp_f32_e32 v165, v165
	v_fma_f32 v62, v62, v170, v228
	v_fma_f32 v63, v63, v162, v228
	v_fma_f32 v64, v64, v171, v228
	v_fma_f32 v65, v65, v163, v228
	v_fma_f32 v58, v58, v214, v228
	v_fma_f32 v59, v59, v164, v228
	v_fma_f32 v60, v60, v215, v228
	v_fma_f32 v61, v61, v165, v228
	v_cvt_pk_bf16_f32 v62, v62, v63
	v_cvt_pk_bf16_f32 v63, v64, v65
	v_cvt_pk_bf16_f32 v64, v58, v59
	v_cvt_pk_bf16_f32 v65, v60, v61
	global_store_dwordx4 v226, v[62:65], s[4:5] offset:256
	s_waitcnt vmcnt(17)
	v_lshlrev_b32_e32 v170, 16, v166
	v_and_b32_e32 v166, 0xffff0000, v166
	v_lshlrev_b32_e32 v171, 16, v167
	v_and_b32_e32 v167, 0xffff0000, v167
	v_lshlrev_b32_e32 v214, 16, v168
	v_and_b32_e32 v168, 0xffff0000, v168
	v_lshlrev_b32_e32 v215, 16, v169
	v_and_b32_e32 v169, 0xffff0000, v169
	v_add_f32_e32 v170, v130, v170
	v_add_f32_e32 v166, v131, v166
	v_add_f32_e32 v171, v132, v171
	v_add_f32_e32 v167, v133, v167
	v_add_f32_e32 v214, v122, v214
	v_add_f32_e32 v168, v123, v168
	v_add_f32_e32 v215, v124, v215
	v_add_f32_e32 v169, v125, v169
	v_mul_f32_e32 v170, 0xbfb8aa3b, v170
	v_mul_f32_e32 v166, 0xbfb8aa3b, v166
	v_mul_f32_e32 v171, 0xbfb8aa3b, v171
	v_mul_f32_e32 v167, 0xbfb8aa3b, v167
	v_mul_f32_e32 v214, 0xbfb8aa3b, v214
	v_mul_f32_e32 v168, 0xbfb8aa3b, v168
	v_mul_f32_e32 v215, 0xbfb8aa3b, v215
	v_mul_f32_e32 v169, 0xbfb8aa3b, v169
	v_exp_f32_e32 v170, v170
	v_exp_f32_e32 v166, v166
	v_exp_f32_e32 v171, v171
	v_exp_f32_e32 v167, v167
	v_exp_f32_e32 v214, v214
	v_exp_f32_e32 v168, v168
	v_exp_f32_e32 v215, v215
	v_exp_f32_e32 v169, v169
	v_add_f32_e32 v170, 1.0, v170
	v_add_f32_e32 v166, 1.0, v166
	v_add_f32_e32 v171, 1.0, v171
	v_add_f32_e32 v167, 1.0, v167
	v_add_f32_e32 v214, 1.0, v214
	v_add_f32_e32 v168, 1.0, v168
	v_add_f32_e32 v215, 1.0, v215
	v_add_f32_e32 v169, 1.0, v169
	v_rcp_f32_e32 v170, v170
	v_rcp_f32_e32 v166, v166
	v_rcp_f32_e32 v171, v171
	v_rcp_f32_e32 v167, v167
	v_rcp_f32_e32 v214, v214
	v_rcp_f32_e32 v168, v168
	v_rcp_f32_e32 v215, v215
	v_rcp_f32_e32 v169, v169
	v_fma_f32 v54, v54, v170, v232
	v_fma_f32 v55, v55, v166, v232
	v_fma_f32 v56, v56, v171, v232
	v_fma_f32 v57, v57, v167, v232
	v_fma_f32 v50, v50, v214, v232
	v_fma_f32 v51, v51, v168, v232
	v_fma_f32 v52, v52, v215, v232
	v_fma_f32 v53, v53, v169, v232
	v_cvt_pk_bf16_f32 v54, v54, v55
	v_cvt_pk_bf16_f32 v55, v56, v57
	v_cvt_pk_bf16_f32 v56, v50, v51
	v_cvt_pk_bf16_f32 v57, v52, v53
	v_add_u32_e32 v225, 0x10000, v226
	global_store_dwordx4 v225, v[54:57], s[4:5] offset:256
	s_waitcnt vmcnt(17)
	v_lshlrev_b32_e32 v170, 16, v190
	v_and_b32_e32 v190, 0xffff0000, v190
	v_lshlrev_b32_e32 v171, 16, v191
	v_and_b32_e32 v191, 0xffff0000, v191
	v_lshlrev_b32_e32 v214, 16, v192
	v_and_b32_e32 v192, 0xffff0000, v192
	v_lshlrev_b32_e32 v215, 16, v193
	v_and_b32_e32 v193, 0xffff0000, v193
	v_add_f32_e32 v170, v130, v170
	v_add_f32_e32 v190, v131, v190
	v_add_f32_e32 v171, v132, v171
	v_add_f32_e32 v191, v133, v191
	v_add_f32_e32 v214, v122, v214
	v_add_f32_e32 v192, v123, v192
	v_add_f32_e32 v215, v124, v215
	v_add_f32_e32 v193, v125, v193
	v_mul_f32_e32 v170, 0xbfb8aa3b, v170
	v_mul_f32_e32 v190, 0xbfb8aa3b, v190
	v_mul_f32_e32 v171, 0xbfb8aa3b, v171
	v_mul_f32_e32 v191, 0xbfb8aa3b, v191
	v_mul_f32_e32 v214, 0xbfb8aa3b, v214
	v_mul_f32_e32 v192, 0xbfb8aa3b, v192
	v_mul_f32_e32 v215, 0xbfb8aa3b, v215
	v_mul_f32_e32 v193, 0xbfb8aa3b, v193
	v_exp_f32_e32 v170, v170
	v_exp_f32_e32 v190, v190
	v_exp_f32_e32 v171, v171
	v_exp_f32_e32 v191, v191
	v_exp_f32_e32 v214, v214
	v_exp_f32_e32 v192, v192
	v_exp_f32_e32 v215, v215
	v_exp_f32_e32 v193, v193
	v_add_f32_e32 v170, 1.0, v170
	v_add_f32_e32 v190, 1.0, v190
	v_add_f32_e32 v171, 1.0, v171
	v_add_f32_e32 v191, 1.0, v191
	v_add_f32_e32 v214, 1.0, v214
	v_add_f32_e32 v192, 1.0, v192
	v_add_f32_e32 v215, 1.0, v215
	v_add_f32_e32 v193, 1.0, v193
	v_rcp_f32_e32 v170, v170
	v_rcp_f32_e32 v190, v190
	v_rcp_f32_e32 v171, v171
	v_rcp_f32_e32 v191, v191
	v_rcp_f32_e32 v214, v214
	v_rcp_f32_e32 v192, v192
	v_rcp_f32_e32 v215, v215
	v_rcp_f32_e32 v193, v193
	v_fma_f32 v46, v46, v170, v236
	v_fma_f32 v47, v47, v190, v236
	v_fma_f32 v48, v48, v171, v236
	v_fma_f32 v49, v49, v191, v236
	v_fma_f32 v42, v42, v214, v236
	v_fma_f32 v43, v43, v192, v236
	v_fma_f32 v44, v44, v215, v236
	v_fma_f32 v45, v45, v193, v236
	v_cvt_pk_bf16_f32 v46, v46, v47
	v_cvt_pk_bf16_f32 v47, v48, v49
	v_cvt_pk_bf16_f32 v48, v42, v43
	v_cvt_pk_bf16_f32 v49, v44, v45
	v_add_u32_e32 v225, 0x20000, v226
	global_store_dwordx4 v225, v[46:49], s[4:5] offset:256
	s_waitcnt vmcnt(17)
; __device__ __forceinline__ void unpack8(const v4u w, float (&o)[8]) { o[0] = bflo(w.x); o[1] = bfhi(w.x); o[2] = bflo(w.y); o[3] = bfhi(w.y); o[4] = bflo(w.z); o[5] = bfhi(w.z); o[6] = bflo(w.w); o[7] = bfhi(w.w); }
; __device__ __forceinline__ v4u pack8(const float (&o)[8]) { v4u w; w.x = pk2(o[0], o[1]); w.y = pk2(o[2], o[3]); w.z = pk2(o[4], o[5]); w.w = pk2(o[6], o[7]); return w; }
; __device__ __forceinline__ float sigmf(float x) { return __builtin_amdgcn_rcpf(1.f + __expf(-x)); }
;     __device__ __forceinline__ void operator()(const f32x4 (&acc)[2][2][4][2], const pg8::Unit& u, int wr, int wc, int fr, int fq_in) const {
;     ...
;                 for (int m = 0; m < 4; ++m) { const size_t row = (size_t)(row0 + ai * 128 + m * 16);
;                     gw_[m] = *(const v4u*)(Gt + row * (2 * D) + goff + col); pw_[m] = first ? (v4u){0u, 0u, 0u, 0u} : *(const v4u*)(O + row * D + col); }
;                 __builtin_amdgcn_sched_barrier(0);
; #pragma unroll
;                 for (int m = 0; m < 4; ++m) { const size_t row = (size_t)(row0 + ai * 128 + m * 16);
;                     float g0[8], p[8]; unpack8(gw_[m], g0); unpack8(pw_[m], p);
;                     float o[8];
; #pragma unroll
;                     for (int q = 0; q < 4; ++q) { o[q] = p[q] + sigmf(g0[q] + b0[q]) * acc[ai][bj][m][0][q]; o[4 + q] = p[4 + q] + sigmf(g0[4 + q] + b0[4 + q]) * acc[ai][bj][m][1][q]; }
;                     *(v4u*)(O + row * D + col) = pack8(o); }
	v_lshlrev_b32_e32 v170, 16, v194
	v_and_b32_e32 v194, 0xffff0000, v194
	v_lshlrev_b32_e32 v171, 16, v195
	v_and_b32_e32 v195, 0xffff0000, v195
	v_lshlrev_b32_e32 v214, 16, v196
	v_and_b32_e32 v196, 0xffff0000, v196
	v_lshlrev_b32_e32 v215, 16, v197
	v_and_b32_e32 v197, 0xffff0000, v197
	v_add_f32_e32 v170, v130, v170
	v_add_f32_e32 v194, v131, v194
	v_add_f32_e32 v171, v132, v171
	v_add_f32_e32 v195, v133, v195
	v_add_f32_e32 v214, v122, v214
	v_add_f32_e32 v196, v123, v196
	v_add_f32_e32 v215, v124, v215
	v_add_f32_e32 v197, v125, v197
	v_mul_f32_e32 v170, 0xbfb8aa3b, v170
	v_mul_f32_e32 v194, 0xbfb8aa3b, v194
	v_mul_f32_e32 v171, 0xbfb8aa3b, v171
	v_mul_f32_e32 v195, 0xbfb8aa3b, v195
	v_mul_f32_e32 v214, 0xbfb8aa3b, v214
	v_mul_f32_e32 v196, 0xbfb8aa3b, v196
	v_mul_f32_e32 v215, 0xbfb8aa3b, v215
	v_mul_f32_e32 v197, 0xbfb8aa3b, v197
	v_exp_f32_e32 v170, v170
	v_exp_f32_e32 v194, v194
	v_exp_f32_e32 v171, v171
	v_exp_f32_e32 v195, v195
	v_exp_f32_e32 v214, v214
	v_exp_f32_e32 v196, v196
	v_exp_f32_e32 v215, v215
	v_exp_f32_e32 v197, v197
	v_add_f32_e32 v170, 1.0, v170
	v_add_f32_e32 v194, 1.0, v194
	v_add_f32_e32 v171, 1.0, v171
	v_add_f32_e32 v195, 1.0, v195
	v_add_f32_e32 v214, 1.0, v214
	v_add_f32_e32 v196, 1.0, v196
	v_add_f32_e32 v215, 1.0, v215
	v_add_f32_e32 v197, 1.0, v197
	v_rcp_f32_e32 v170, v170
	v_rcp_f32_e32 v194, v194
	v_rcp_f32_e32 v171, v171
	v_rcp_f32_e32 v195, v195
	v_rcp_f32_e32 v214, v214
	v_rcp_f32_e32 v196, v196
	v_rcp_f32_e32 v215, v215
	v_rcp_f32_e32 v197, v197
	v_fma_f32 v38, v38, v170, v240
	v_fma_f32 v39, v39, v194, v240
	v_fma_f32 v40, v40, v171, v240
	v_fma_f32 v41, v41, v195, v240
	v_fma_f32 v34, v34, v214, v240
	v_fma_f32 v35, v35, v196, v240
	v_fma_f32 v36, v36, v215, v240
	v_fma_f32 v37, v37, v197, v240
	v_cvt_pk_bf16_f32 v38, v38, v39
	v_cvt_pk_bf16_f32 v39, v40, v41
	v_cvt_pk_bf16_f32 v40, v34, v35
	v_cvt_pk_bf16_f32 v41, v36, v37
	v_add_u32_e32 v225, 0x30000, v226
	global_store_dwordx4 v225, v[38:41], s[4:5] offset:256
	s_waitcnt vmcnt(17)
	v_lshlrev_b32_e32 v170, 16, v198
	v_and_b32_e32 v198, 0xffff0000, v198
	v_lshlrev_b32_e32 v171, 16, v199
	v_and_b32_e32 v199, 0xffff0000, v199
	v_lshlrev_b32_e32 v214, 16, v200
	v_and_b32_e32 v200, 0xffff0000, v200
	v_lshlrev_b32_e32 v215, 16, v201
	v_and_b32_e32 v201, 0xffff0000, v201
	v_add_f32_e32 v170, v130, v170
	v_add_f32_e32 v198, v131, v198
	v_add_f32_e32 v171, v132, v171
	v_add_f32_e32 v199, v133, v199
	v_add_f32_e32 v214, v122, v214
	v_add_f32_e32 v200, v123, v200
	v_add_f32_e32 v215, v124, v215
	v_add_f32_e32 v201, v125, v201
	v_mul_f32_e32 v170, 0xbfb8aa3b, v170
	v_mul_f32_e32 v198, 0xbfb8aa3b, v198
	v_mul_f32_e32 v171, 0xbfb8aa3b, v171
	v_mul_f32_e32 v199, 0xbfb8aa3b, v199
	v_mul_f32_e32 v214, 0xbfb8aa3b, v214
	v_mul_f32_e32 v200, 0xbfb8aa3b, v200
	v_mul_f32_e32 v215, 0xbfb8aa3b, v215
	v_mul_f32_e32 v201, 0xbfb8aa3b, v201
	v_exp_f32_e32 v170, v170
	v_exp_f32_e32 v198, v198
	v_exp_f32_e32 v171, v171
	v_exp_f32_e32 v199, v199
	v_exp_f32_e32 v214, v214
	v_exp_f32_e32 v200, v200
	v_exp_f32_e32 v215, v215
	v_exp_f32_e32 v201, v201
	v_add_f32_e32 v170, 1.0, v170
	v_add_f32_e32 v198, 1.0, v198
	v_add_f32_e32 v171, 1.0, v171
	v_add_f32_e32 v199, 1.0, v199
	v_add_f32_e32 v214, 1.0, v214
	v_add_f32_e32 v200, 1.0, v200
	v_add_f32_e32 v215, 1.0, v215
	v_add_f32_e32 v201, 1.0, v201
	v_rcp_f32_e32 v170, v170
	v_rcp_f32_e32 v198, v198
	v_rcp_f32_e32 v171, v171
	v_rcp_f32_e32 v199, v199
	v_rcp_f32_e32 v214, v214
	v_rcp_f32_e32 v200, v200
	v_rcp_f32_e32 v215, v215
	v_rcp_f32_e32 v201, v201
	v_fma_f32 v30, v30, v170, v228
	v_fma_f32 v31, v31, v198, v228
	v_fma_f32 v32, v32, v171, v228
	v_fma_f32 v33, v33, v199, v228
	v_fma_f32 v26, v26, v214, v228
	v_fma_f32 v27, v27, v200, v228
	v_fma_f32 v28, v28, v215, v228
	v_fma_f32 v29, v29, v201, v228
	v_cvt_pk_bf16_f32 v30, v30, v31
	v_cvt_pk_bf16_f32 v31, v32, v33
	v_cvt_pk_bf16_f32 v32, v26, v27
	v_cvt_pk_bf16_f32 v33, v28, v29
	v_add_u32_e32 v225, 0x80000, v226
	global_store_dwordx4 v225, v[30:33], s[4:5] offset:256
	s_waitcnt vmcnt(17)
	v_lshlrev_b32_e32 v170, 16, v202
	v_and_b32_e32 v202, 0xffff0000, v202
	v_lshlrev_b32_e32 v171, 16, v203
	v_and_b32_e32 v203, 0xffff0000, v203
	v_lshlrev_b32_e32 v214, 16, v204
	v_and_b32_e32 v204, 0xffff0000, v204
	v_lshlrev_b32_e32 v215, 16, v205
	v_and_b32_e32 v205, 0xffff0000, v205
	v_add_f32_e32 v170, v130, v170
	v_add_f32_e32 v202, v131, v202
	v_add_f32_e32 v171, v132, v171
	v_add_f32_e32 v203, v133, v203
	v_add_f32_e32 v214, v122, v214
	v_add_f32_e32 v204, v123, v204
	v_add_f32_e32 v215, v124, v215
	v_add_f32_e32 v205, v125, v205
	v_mul_f32_e32 v170, 0xbfb8aa3b, v170
	v_mul_f32_e32 v202, 0xbfb8aa3b, v202
	v_mul_f32_e32 v171, 0xbfb8aa3b, v171
	v_mul_f32_e32 v203, 0xbfb8aa3b, v203
	v_mul_f32_e32 v214, 0xbfb8aa3b, v214
	v_mul_f32_e32 v204, 0xbfb8aa3b, v204
	v_mul_f32_e32 v215, 0xbfb8aa3b, v215
	v_mul_f32_e32 v205, 0xbfb8aa3b, v205
	v_exp_f32_e32 v170, v170
	v_exp_f32_e32 v202, v202
	v_exp_f32_e32 v171, v171
	v_exp_f32_e32 v203, v203
	v_exp_f32_e32 v214, v214
	v_exp_f32_e32 v204, v204
	v_exp_f32_e32 v215, v215
	v_exp_f32_e32 v205, v205
	v_add_f32_e32 v170, 1.0, v170
	v_add_f32_e32 v202, 1.0, v202
	v_add_f32_e32 v171, 1.0, v171
	v_add_f32_e32 v203, 1.0, v203
	v_add_f32_e32 v214, 1.0, v214
	v_add_f32_e32 v204, 1.0, v204
	v_add_f32_e32 v215, 1.0, v215
	v_add_f32_e32 v205, 1.0, v205
	v_rcp_f32_e32 v170, v170
	v_rcp_f32_e32 v202, v202
	v_rcp_f32_e32 v171, v171
	v_rcp_f32_e32 v203, v203
	v_rcp_f32_e32 v214, v214
	v_rcp_f32_e32 v204, v204
	v_rcp_f32_e32 v215, v215
	v_rcp_f32_e32 v205, v205
	v_fma_f32 v22, v22, v170, v232
	v_fma_f32 v23, v23, v202, v232
	v_fma_f32 v24, v24, v171, v232
	v_fma_f32 v25, v25, v203, v232
	v_fma_f32 v18, v18, v214, v232
	v_fma_f32 v19, v19, v204, v232
	v_fma_f32 v20, v20, v215, v232
	v_fma_f32 v21, v21, v205, v232
	v_cvt_pk_bf16_f32 v22, v22, v23
	v_cvt_pk_bf16_f32 v23, v24, v25
	v_cvt_pk_bf16_f32 v24, v18, v19
	v_cvt_pk_bf16_f32 v25, v20, v21
	v_add_u32_e32 v225, 0x90000, v226
	global_store_dwordx4 v225, v[22:25], s[4:5] offset:256
	s_waitcnt vmcnt(17)
; __device__ __forceinline__ void unpack8(const v4u w, float (&o)[8]) { o[0] = bflo(w.x); o[1] = bfhi(w.x); o[2] = bflo(w.y); o[3] = bfhi(w.y); o[4] = bflo(w.z); o[5] = bfhi(w.z); o[6] = bflo(w.w); o[7] = bfhi(w.w); }
; __device__ __forceinline__ v4u pack8(const float (&o)[8]) { v4u w; w.x = pk2(o[0], o[1]); w.y = pk2(o[2], o[3]); w.z = pk2(o[4], o[5]); w.w = pk2(o[6], o[7]); return w; }
; __device__ __forceinline__ float sigmf(float x) { return __builtin_amdgcn_rcpf(1.f + __expf(-x)); }
;     __device__ __forceinline__ void operator()(const f32x4 (&acc)[2][2][4][2], const pg8::Unit& u, int wr, int wc, int fr, int fq_in) const {
;         int fq = fq_in; asm volatile("" : "+v"(fq));
;         const int row0 = u.pm * 256 + wr * 64 + fr, col0 = u.pn * 256 + wc * 32 + 8 * fq; const bool first = u.sel == 0; const int goff = first ? 0 : D;
; #pragma unroll
;         for (int bj = 0; bj < 2; ++bj) {
;             const int col = col0 + bj * 128;
;             float b0[8];
;             { const f32x4 t0 = *(const f32x4*)(bg + goff + col), t1 = *(const f32x4*)(bg + goff + col + 4);
; #pragma unroll
;               for (int q = 0; q < 4; ++q) { b0[q] = t0[q]; b0[4 + q] = t1[q]; } }
; #pragma unroll
;             for (int ai = 0; ai < 2; ++ai) {
;                 v4u gw_[4], pw_[4];
; #pragma unroll
;                 for (int m = 0; m < 4; ++m) { const size_t row = (size_t)(row0 + ai * 128 + m * 16);
;                     gw_[m] = *(const v4u*)(Gt + row * (2 * D) + goff + col); pw_[m] = first ? (v4u){0u, 0u, 0u, 0u} : *(const v4u*)(O + row * D + col); }
;                 __builtin_amdgcn_sched_barrier(0);
; #pragma unroll
;                 for (int m = 0; m < 4; ++m) { const size_t row = (size_t)(row0 + ai * 128 + m * 16);
;                     float g0[8], p[8]; unpack8(gw_[m], g0); unpack8(pw_[m], p);
;                     float o[8];
; #pragma unroll
;                     for (int q = 0; q < 4; ++q) { o[q] = p[q] + sigmf(g0[q] + b0[q]) * acc[ai][bj][m][0][q]; o[4 + q] = p[4 + q] + sigmf(g0[4 + q] + b0[4 + q]) * acc[ai][bj][m][1][q]; }
;                     *(v4u*)(O + row * D + col) = pack8(o); }
;             }
;         }
	v_lshlrev_b32_e32 v170, 16, v206
	v_and_b32_e32 v206, 0xffff0000, v206
	v_lshlrev_b32_e32 v171, 16, v207
	v_and_b32_e32 v207, 0xffff0000, v207
	v_lshlrev_b32_e32 v214, 16, v208
	v_and_b32_e32 v208, 0xffff0000, v208
	v_lshlrev_b32_e32 v215, 16, v209
	v_and_b32_e32 v209, 0xffff0000, v209
	v_add_f32_e32 v170, v130, v170
	v_add_f32_e32 v206, v131, v206
	v_add_f32_e32 v171, v132, v171
	v_add_f32_e32 v207, v133, v207
	v_add_f32_e32 v214, v122, v214
	v_add_f32_e32 v208, v123, v208
	v_add_f32_e32 v215, v124, v215
	v_add_f32_e32 v209, v125, v209
	v_mul_f32_e32 v170, 0xbfb8aa3b, v170
	v_mul_f32_e32 v206, 0xbfb8aa3b, v206
	v_mul_f32_e32 v171, 0xbfb8aa3b, v171
	v_mul_f32_e32 v207, 0xbfb8aa3b, v207
	v_mul_f32_e32 v214, 0xbfb8aa3b, v214
	v_mul_f32_e32 v208, 0xbfb8aa3b, v208
	v_mul_f32_e32 v215, 0xbfb8aa3b, v215
	v_mul_f32_e32 v209, 0xbfb8aa3b, v209
	v_exp_f32_e32 v170, v170
	v_exp_f32_e32 v206, v206
	v_exp_f32_e32 v171, v171
	v_exp_f32_e32 v207, v207
	v_exp_f32_e32 v214, v214
	v_exp_f32_e32 v208, v208
	v_exp_f32_e32 v215, v215
	v_exp_f32_e32 v209, v209
	v_add_f32_e32 v170, 1.0, v170
	v_add_f32_e32 v206, 1.0, v206
	v_add_f32_e32 v171, 1.0, v171
	v_add_f32_e32 v207, 1.0, v207
	v_add_f32_e32 v214, 1.0, v214
	v_add_f32_e32 v208, 1.0, v208
	v_add_f32_e32 v215, 1.0, v215
	v_add_f32_e32 v209, 1.0, v209
	v_rcp_f32_e32 v170, v170
	v_rcp_f32_e32 v206, v206
	v_rcp_f32_e32 v171, v171
	v_rcp_f32_e32 v207, v207
	v_rcp_f32_e32 v214, v214
	v_rcp_f32_e32 v208, v208
	v_rcp_f32_e32 v215, v215
	v_rcp_f32_e32 v209, v209
	v_fma_f32 v14, v14, v170, v236
	v_fma_f32 v15, v15, v206, v236
	v_fma_f32 v16, v16, v171, v236
	v_fma_f32 v17, v17, v207, v236
	v_fma_f32 v10, v10, v214, v236
	v_fma_f32 v11, v11, v208, v236
	v_fma_f32 v12, v12, v215, v236
	v_fma_f32 v13, v13, v209, v236
	v_cvt_pk_bf16_f32 v14, v14, v15
	v_cvt_pk_bf16_f32 v15, v16, v17
	v_cvt_pk_bf16_f32 v16, v10, v11
	v_cvt_pk_bf16_f32 v17, v12, v13
	v_add_u32_e32 v225, 0xa0000, v226
	global_store_dwordx4 v225, v[14:17], s[4:5] offset:256
	s_waitcnt vmcnt(17)
	v_lshlrev_b32_e32 v170, 16, v210
	v_and_b32_e32 v210, 0xffff0000, v210
	v_lshlrev_b32_e32 v171, 16, v211
	v_and_b32_e32 v211, 0xffff0000, v211
	v_lshlrev_b32_e32 v214, 16, v212
	v_and_b32_e32 v212, 0xffff0000, v212
	v_lshlrev_b32_e32 v215, 16, v213
	v_and_b32_e32 v213, 0xffff0000, v213
	v_add_f32_e32 v170, v130, v170
	v_add_f32_e32 v210, v131, v210
	v_add_f32_e32 v171, v132, v171
	v_add_f32_e32 v211, v133, v211
	v_add_f32_e32 v214, v122, v214
	v_add_f32_e32 v212, v123, v212
	v_add_f32_e32 v215, v124, v215
	v_add_f32_e32 v213, v125, v213
	v_mul_f32_e32 v170, 0xbfb8aa3b, v170
	v_mul_f32_e32 v210, 0xbfb8aa3b, v210
	v_mul_f32_e32 v171, 0xbfb8aa3b, v171
	v_mul_f32_e32 v211, 0xbfb8aa3b, v211
	v_mul_f32_e32 v214, 0xbfb8aa3b, v214
	v_mul_f32_e32 v212, 0xbfb8aa3b, v212
	v_mul_f32_e32 v215, 0xbfb8aa3b, v215
	v_mul_f32_e32 v213, 0xbfb8aa3b, v213
	v_exp_f32_e32 v170, v170
	v_exp_f32_e32 v210, v210
	v_exp_f32_e32 v171, v171
	v_exp_f32_e32 v211, v211
	v_exp_f32_e32 v214, v214
	v_exp_f32_e32 v212, v212
	v_exp_f32_e32 v215, v215
	v_exp_f32_e32 v213, v213
	v_add_f32_e32 v170, 1.0, v170
	v_add_f32_e32 v210, 1.0, v210
	v_add_f32_e32 v171, 1.0, v171
	v_add_f32_e32 v211, 1.0, v211
	v_add_f32_e32 v214, 1.0, v214
	v_add_f32_e32 v212, 1.0, v212
	v_add_f32_e32 v215, 1.0, v215
	v_add_f32_e32 v213, 1.0, v213
	v_rcp_f32_e32 v170, v170
	v_rcp_f32_e32 v210, v210
	v_rcp_f32_e32 v171, v171
	v_rcp_f32_e32 v211, v211
	v_rcp_f32_e32 v214, v214
	v_rcp_f32_e32 v212, v212
	v_rcp_f32_e32 v215, v215
	v_rcp_f32_e32 v213, v213
	v_fma_f32 v6, v6, v170, v240
	v_fma_f32 v7, v7, v210, v240
	v_fma_f32 v8, v8, v171, v240
	v_fma_f32 v9, v9, v211, v240
	v_fma_f32 v2, v2, v214, v240
	v_fma_f32 v3, v3, v212, v240
	v_fma_f32 v4, v4, v215, v240
	v_fma_f32 v5, v5, v213, v240
	v_cvt_pk_bf16_f32 v6, v6, v7
	v_cvt_pk_bf16_f32 v7, v8, v9
	v_cvt_pk_bf16_f32 v8, v2, v3
	v_cvt_pk_bf16_f32 v9, v4, v5
	v_add_u32_e32 v225, 0xb0000, v226
	global_store_dwordx4 v225, v[6:9], s[4:5] offset:256
	s_branch .Lepi6_done
.Lepi6_second:
	global_load_dwordx4 v[244:247], v252, s[0:1]
	global_load_dwordx4 v[248:251], v252, s[0:1] offset:16
	global_load_dwordx4 v[114:117], v227, s[98:99]
	global_load_dwordx4 v[228:231], v226, s[4:5]
	v_add_u32_e32 v254, 0x4000, v227
	global_load_dwordx4 v[118:121], v254, s[98:99]
	v_add_u32_e32 v253, 0x10000, v226
	global_load_dwordx4 v[232:235], v253, s[4:5]
	v_add_u32_e32 v254, 0x8000, v227
	global_load_dwordx4 v[138:141], v254, s[98:99]
	v_add_u32_e32 v253, 0x20000, v226
	global_load_dwordx4 v[236:239], v253, s[4:5]
	v_add_u32_e32 v254, 0xc000, v227
	global_load_dwordx4 v[142:145], v254, s[98:99]
	v_add_u32_e32 v253, 0x30000, v226
	global_load_dwordx4 v[240:243], v253, s[4:5]
	v_add_u32_e32 v254, 0x10000, v227
	global_load_dwordx4 v[146:149], v254, s[98:99]
	v_add_u32_e32 v254, 0x14000, v227
	global_load_dwordx4 v[150:153], v254, s[98:99]
	v_add_u32_e32 v254, 0x18000, v227
	global_load_dwordx4 v[154:157], v254, s[98:99]
	v_add_u32_e32 v254, 0x1c000, v227
	global_load_dwordx4 v[158:161], v254, s[98:99]
	v_add_u32_e32 v254, 0x2000, v227
	global_load_dwordx4 v[162:165], v254, s[98:99]
	v_add_u32_e32 v254, 0x6000, v227
	global_load_dwordx4 v[166:169], v254, s[98:99]
	v_add_u32_e32 v254, 0xa000, v227
	global_load_dwordx4 v[190:193], v254, s[98:99]
	v_add_u32_e32 v254, 0xe000, v227
	global_load_dwordx4 v[194:197], v254, s[98:99]
	v_add_u32_e32 v254, 0x12000, v227
	global_load_dwordx4 v[198:201], v254, s[98:99]
	v_add_u32_e32 v254, 0x16000, v227
	global_load_dwordx4 v[202:205], v254, s[98:99]
	v_add_u32_e32 v254, 0x1a000, v227
	global_load_dwordx4 v[206:209], v254, s[98:99]
	v_add_u32_e32 v254, 0x1e000, v227
	global_load_dwordx4 v[210:213], v254, s[98:99]
	s_waitcnt vmcnt(20)
; __device__ __forceinline__ v4u pack8(const float (&o)[8]) { v4u w; w.x = pk2(o[0], o[1]); w.y = pk2(o[2], o[3]); w.z = pk2(o[4], o[5]); w.w = pk2(o[6], o[7]); return w; }
; __device__ __forceinline__ float sigmf(float x) { return __builtin_amdgcn_rcpf(1.f + __expf(-x)); }
; __device__ __forceinline__ unsigned pk2(float lo, float hi) { typedef float f2v __attribute__((ext_vector_type(2))); typedef __bf16 b2v __attribute__((ext_vector_type(2))); const f2v v = {lo, hi}; return __builtin_bit_cast(unsigned, __builtin_convertvector(v, b2v)); }
; __device__ __forceinline__ void unpack8(const v4u w, float (&o)[8]) { o[0] = bflo(w.x); o[1] = bfhi(w.x); o[2] = bflo(w.y); o[3] = bfhi(w.y); o[4] = bflo(w.z); o[5] = bfhi(w.z); o[6] = bflo(w.w); o[7] = bfhi(w.w); }
;     __device__ __forceinline__ void operator()(const f32x4 (&acc)[2][2][4][2], const pg8::Unit& u, int wr, int wc, int fr, int fq_in) const {
;     ...
;                 for (int m = 0; m < 4; ++m) { const size_t row = (size_t)(row0 + ai * 128 + m * 16);
;                     gw_[m] = *(const v4u*)(Gt + row * (2 * D) + goff + col); pw_[m] = first ? (v4u){0u, 0u, 0u, 0u} : *(const v4u*)(O + row * D + col); }
;                 __builtin_amdgcn_sched_barrier(0);
; #pragma unroll
;                 for (int m = 0; m < 4; ++m) { const size_t row = (size_t)(row0 + ai * 128 + m * 16);
;                     float g0[8], p[8]; unpack8(gw_[m], g0); unpack8(pw_[m], p);
;                     float o[8];
; #pragma unroll
;                     for (int q = 0; q < 4; ++q) { o[q] = p[q] + sigmf(g0[q] + b0[q]) * acc[ai][bj][m][0][q]; o[4 + q] = p[4 + q] + sigmf(g0[4 + q] + b0[4 + q]) * acc[ai][bj][m][1][q]; }
;                     *(v4u*)(O + row * D + col) = pack8(o); }
	s_waitcnt vmcnt(19)
	v_lshlrev_b32_e32 v170, 16, v114
	v_and_b32_e32 v114, 0xffff0000, v114
	v_lshlrev_b32_e32 v171, 16, v115
	v_and_b32_e32 v115, 0xffff0000, v115
	v_lshlrev_b32_e32 v214, 16, v116
	v_and_b32_e32 v116, 0xffff0000, v116
	v_lshlrev_b32_e32 v215, 16, v117
	v_and_b32_e32 v117, 0xffff0000, v117
	v_add_f32_e32 v170, v244, v170
	v_add_f32_e32 v114, v245, v114
	v_add_f32_e32 v171, v246, v171
	v_add_f32_e32 v115, v247, v115
	v_add_f32_e32 v214, v248, v214
	v_add_f32_e32 v116, v249, v116
	v_add_f32_e32 v215, v250, v215
	v_add_f32_e32 v117, v251, v117
	v_mul_f32_e32 v170, 0xbfb8aa3b, v170
	v_mul_f32_e32 v114, 0xbfb8aa3b, v114
	v_mul_f32_e32 v171, 0xbfb8aa3b, v171
	v_mul_f32_e32 v115, 0xbfb8aa3b, v115
	v_mul_f32_e32 v214, 0xbfb8aa3b, v214
	v_mul_f32_e32 v116, 0xbfb8aa3b, v116
	v_mul_f32_e32 v215, 0xbfb8aa3b, v215
	v_mul_f32_e32 v117, 0xbfb8aa3b, v117
	v_exp_f32_e32 v170, v170
	v_exp_f32_e32 v114, v114
	v_exp_f32_e32 v171, v171
	v_exp_f32_e32 v115, v115
	v_exp_f32_e32 v214, v214
	v_exp_f32_e32 v116, v116
	v_exp_f32_e32 v215, v215
	v_exp_f32_e32 v117, v117
	v_add_f32_e32 v170, 1.0, v170
	v_add_f32_e32 v114, 1.0, v114
	v_add_f32_e32 v171, 1.0, v171
	v_add_f32_e32 v115, 1.0, v115
	v_add_f32_e32 v214, 1.0, v214
	v_add_f32_e32 v116, 1.0, v116
	v_add_f32_e32 v215, 1.0, v215
	v_add_f32_e32 v117, 1.0, v117
	v_rcp_f32_e32 v170, v170
	v_rcp_f32_e32 v114, v114
	v_rcp_f32_e32 v171, v171
	v_rcp_f32_e32 v115, v115
	v_rcp_f32_e32 v214, v214
	v_rcp_f32_e32 v116, v116
	v_rcp_f32_e32 v215, v215
	v_rcp_f32_e32 v117, v117
	s_waitcnt vmcnt(18)
	v_lshlrev_b32_e32 v221, 16, v228
	v_and_b32_e32 v228, 0xffff0000, v228
	v_lshlrev_b32_e32 v222, 16, v229
	v_and_b32_e32 v229, 0xffff0000, v229
	v_lshlrev_b32_e32 v223, 16, v230
	v_and_b32_e32 v230, 0xffff0000, v230
	v_lshlrev_b32_e32 v224, 16, v231
	v_and_b32_e32 v231, 0xffff0000, v231
	v_fma_f32 v134, v134, v170, v221
	v_fma_f32 v135, v135, v114, v228
	v_fma_f32 v136, v136, v171, v222
	v_fma_f32 v137, v137, v115, v229
	v_fma_f32 v130, v130, v214, v223
	v_fma_f32 v131, v131, v116, v230
	v_fma_f32 v132, v132, v215, v224
	v_fma_f32 v133, v133, v117, v231
	v_cvt_pk_bf16_f32 v134, v134, v135
	v_cvt_pk_bf16_f32 v135, v136, v137
	v_cvt_pk_bf16_f32 v136, v130, v131
	v_cvt_pk_bf16_f32 v137, v132, v133
	v_add_u32_e32 v253, 0x80000, v226
	global_load_dwordx4 v[228:231], v253, s[4:5]
	global_store_dwordx4 v226, v[134:137], s[4:5]
	s_waitcnt vmcnt(19)
	v_lshlrev_b32_e32 v170, 16, v118
	v_and_b32_e32 v118, 0xffff0000, v118
	v_lshlrev_b32_e32 v171, 16, v119
	v_and_b32_e32 v119, 0xffff0000, v119
	v_lshlrev_b32_e32 v214, 16, v120
	v_and_b32_e32 v120, 0xffff0000, v120
	v_lshlrev_b32_e32 v215, 16, v121
	v_and_b32_e32 v121, 0xffff0000, v121
	v_add_f32_e32 v170, v244, v170
	v_add_f32_e32 v118, v245, v118
	v_add_f32_e32 v171, v246, v171
	v_add_f32_e32 v119, v247, v119
	v_add_f32_e32 v214, v248, v214
	v_add_f32_e32 v120, v249, v120
	v_add_f32_e32 v215, v250, v215
	v_add_f32_e32 v121, v251, v121
	v_mul_f32_e32 v170, 0xbfb8aa3b, v170
	v_mul_f32_e32 v118, 0xbfb8aa3b, v118
	v_mul_f32_e32 v171, 0xbfb8aa3b, v171
	v_mul_f32_e32 v119, 0xbfb8aa3b, v119
	v_mul_f32_e32 v214, 0xbfb8aa3b, v214
	v_mul_f32_e32 v120, 0xbfb8aa3b, v120
	v_mul_f32_e32 v215, 0xbfb8aa3b, v215
	v_mul_f32_e32 v121, 0xbfb8aa3b, v121
	v_exp_f32_e32 v170, v170
	v_exp_f32_e32 v118, v118
	v_exp_f32_e32 v171, v171
	v_exp_f32_e32 v119, v119
	v_exp_f32_e32 v214, v214
	v_exp_f32_e32 v120, v120
	v_exp_f32_e32 v215, v215
	v_exp_f32_e32 v121, v121
	v_add_f32_e32 v170, 1.0, v170
	v_add_f32_e32 v118, 1.0, v118
	v_add_f32_e32 v171, 1.0, v171
	v_add_f32_e32 v119, 1.0, v119
	v_add_f32_e32 v214, 1.0, v214
	v_add_f32_e32 v120, 1.0, v120
	v_add_f32_e32 v215, 1.0, v215
	v_add_f32_e32 v121, 1.0, v121
	v_rcp_f32_e32 v170, v170
	v_rcp_f32_e32 v118, v118
	v_rcp_f32_e32 v171, v171
	v_rcp_f32_e32 v119, v119
	v_rcp_f32_e32 v214, v214
	v_rcp_f32_e32 v120, v120
	v_rcp_f32_e32 v215, v215
	v_rcp_f32_e32 v121, v121
	s_waitcnt vmcnt(18)
	v_lshlrev_b32_e32 v221, 16, v232
	v_and_b32_e32 v232, 0xffff0000, v232
	v_lshlrev_b32_e32 v222, 16, v233
	v_and_b32_e32 v233, 0xffff0000, v233
	v_lshlrev_b32_e32 v223, 16, v234
	v_and_b32_e32 v234, 0xffff0000, v234
	v_lshlrev_b32_e32 v224, 16, v235
	v_and_b32_e32 v235, 0xffff0000, v235
	v_fma_f32 v126, v126, v170, v221
	v_fma_f32 v127, v127, v118, v232
	v_fma_f32 v128, v128, v171, v222
	v_fma_f32 v129, v129, v119, v233
	v_fma_f32 v122, v122, v214, v223
	v_fma_f32 v123, v123, v120, v234
	v_fma_f32 v124, v124, v215, v224
	v_fma_f32 v125, v125, v121, v235
	v_cvt_pk_bf16_f32 v126, v126, v127
	v_cvt_pk_bf16_f32 v127, v128, v129
	v_cvt_pk_bf16_f32 v128, v122, v123
	v_cvt_pk_bf16_f32 v129, v124, v125
	v_add_u32_e32 v253, 0x90000, v226
	global_load_dwordx4 v[232:235], v253, s[4:5]
	v_add_u32_e32 v225, 0x10000, v226
	global_store_dwordx4 v225, v[126:129], s[4:5]
	global_load_dwordx4 v[130:133], v252, s[0:1] offset:512
	global_load_dwordx4 v[122:125], v252, s[0:1] offset:528
	s_waitcnt vmcnt(21)
; __device__ __forceinline__ v4u pack8(const float (&o)[8]) { v4u w; w.x = pk2(o[0], o[1]); w.y = pk2(o[2], o[3]); w.z = pk2(o[4], o[5]); w.w = pk2(o[6], o[7]); return w; }
; __device__ __forceinline__ float sigmf(float x) { return __builtin_amdgcn_rcpf(1.f + __expf(-x)); }
; __device__ __forceinline__ unsigned pk2(float lo, float hi) { typedef float f2v __attribute__((ext_vector_type(2))); typedef __bf16 b2v __attribute__((ext_vector_type(2))); const f2v v = {lo, hi}; return __builtin_bit_cast(unsigned, __builtin_convertvector(v, b2v)); }
; __device__ __forceinline__ void unpack8(const v4u w, float (&o)[8]) { o[0] = bflo(w.x); o[1] = bfhi(w.x); o[2] = bflo(w.y); o[3] = bfhi(w.y); o[4] = bflo(w.z); o[5] = bfhi(w.z); o[6] = bflo(w.w); o[7] = bfhi(w.w); }
;     __device__ __forceinline__ void operator()(const f32x4 (&acc)[2][2][4][2], const pg8::Unit& u, int wr, int wc, int fr, int fq_in) const {
;     ...
;                 for (int m = 0; m < 4; ++m) { const size_t row = (size_t)(row0 + ai * 128 + m * 16);
;                     gw_[m] = *(const v4u*)(Gt + row * (2 * D) + goff + col); pw_[m] = first ? (v4u){0u, 0u, 0u, 0u} : *(const v4u*)(O + row * D + col); }
;                 __builtin_amdgcn_sched_barrier(0);
; #pragma unroll
;                 for (int m = 0; m < 4; ++m) { const size_t row = (size_t)(row0 + ai * 128 + m * 16);
;                     float g0[8], p[8]; unpack8(gw_[m], g0); unpack8(pw_[m], p);
;                     float o[8];
; #pragma unroll
;                     for (int q = 0; q < 4; ++q) { o[q] = p[q] + sigmf(g0[q] + b0[q]) * acc[ai][bj][m][0][q]; o[4 + q] = p[4 + q] + sigmf(g0[4 + q] + b0[4 + q]) * acc[ai][bj][m][1][q]; }
;                     *(v4u*)(O + row * D + col) = pack8(o); }
	v_lshlrev_b32_e32 v170, 16, v138
	v_and_b32_e32 v138, 0xffff0000, v138
	v_lshlrev_b32_e32 v171, 16, v139
	v_and_b32_e32 v139, 0xffff0000, v139
	v_lshlrev_b32_e32 v214, 16, v140
	v_and_b32_e32 v140, 0xffff0000, v140
	v_lshlrev_b32_e32 v215, 16, v141
	v_and_b32_e32 v141, 0xffff0000, v141
	v_add_f32_e32 v170, v244, v170
	v_add_f32_e32 v138, v245, v138
	v_add_f32_e32 v171, v246, v171
	v_add_f32_e32 v139, v247, v139
	v_add_f32_e32 v214, v248, v214
	v_add_f32_e32 v140, v249, v140
	v_add_f32_e32 v215, v250, v215
	v_add_f32_e32 v141, v251, v141
	v_mul_f32_e32 v170, 0xbfb8aa3b, v170
	v_mul_f32_e32 v138, 0xbfb8aa3b, v138
	v_mul_f32_e32 v171, 0xbfb8aa3b, v171
	v_mul_f32_e32 v139, 0xbfb8aa3b, v139
	v_mul_f32_e32 v214, 0xbfb8aa3b, v214
	v_mul_f32_e32 v140, 0xbfb8aa3b, v140
	v_mul_f32_e32 v215, 0xbfb8aa3b, v215
	v_mul_f32_e32 v141, 0xbfb8aa3b, v141
	v_exp_f32_e32 v170, v170
	v_exp_f32_e32 v138, v138
	v_exp_f32_e32 v171, v171
	v_exp_f32_e32 v139, v139
	v_exp_f32_e32 v214, v214
	v_exp_f32_e32 v140, v140
	v_exp_f32_e32 v215, v215
	v_exp_f32_e32 v141, v141
	v_add_f32_e32 v170, 1.0, v170
	v_add_f32_e32 v138, 1.0, v138
	v_add_f32_e32 v171, 1.0, v171
	v_add_f32_e32 v139, 1.0, v139
	v_add_f32_e32 v214, 1.0, v214
	v_add_f32_e32 v140, 1.0, v140
	v_add_f32_e32 v215, 1.0, v215
	v_add_f32_e32 v141, 1.0, v141
	v_rcp_f32_e32 v170, v170
	v_rcp_f32_e32 v138, v138
	v_rcp_f32_e32 v171, v171
	v_rcp_f32_e32 v139, v139
	v_rcp_f32_e32 v214, v214
	v_rcp_f32_e32 v140, v140
	v_rcp_f32_e32 v215, v215
	v_rcp_f32_e32 v141, v141
	s_waitcnt vmcnt(20)
	v_lshlrev_b32_e32 v221, 16, v236
	v_and_b32_e32 v236, 0xffff0000, v236
	v_lshlrev_b32_e32 v222, 16, v237
	v_and_b32_e32 v237, 0xffff0000, v237
	v_lshlrev_b32_e32 v223, 16, v238
	v_and_b32_e32 v238, 0xffff0000, v238
	v_lshlrev_b32_e32 v224, 16, v239
	v_and_b32_e32 v239, 0xffff0000, v239
	v_fma_f32 v110, v110, v170, v221
	v_fma_f32 v111, v111, v138, v236
	v_fma_f32 v112, v112, v171, v222
	v_fma_f32 v113, v113, v139, v237
	v_fma_f32 v106, v106, v214, v223
	v_fma_f32 v107, v107, v140, v238
	v_fma_f32 v108, v108, v215, v224
	v_fma_f32 v109, v109, v141, v239
	v_cvt_pk_bf16_f32 v110, v110, v111
	v_cvt_pk_bf16_f32 v111, v112, v113
	v_cvt_pk_bf16_f32 v112, v106, v107
	v_cvt_pk_bf16_f32 v113, v108, v109
	v_add_u32_e32 v253, 0xa0000, v226
	global_load_dwordx4 v[236:239], v253, s[4:5]
	v_add_u32_e32 v225, 0x20000, v226
	global_store_dwordx4 v225, v[110:113], s[4:5]
	s_waitcnt vmcnt(21)
	v_lshlrev_b32_e32 v170, 16, v142
	v_and_b32_e32 v142, 0xffff0000, v142
	v_lshlrev_b32_e32 v171, 16, v143
	v_and_b32_e32 v143, 0xffff0000, v143
	v_lshlrev_b32_e32 v214, 16, v144
	v_and_b32_e32 v144, 0xffff0000, v144
	v_lshlrev_b32_e32 v215, 16, v145
	v_and_b32_e32 v145, 0xffff0000, v145
	v_add_f32_e32 v170, v244, v170
	v_add_f32_e32 v142, v245, v142
	v_add_f32_e32 v171, v246, v171
	v_add_f32_e32 v143, v247, v143
	v_add_f32_e32 v214, v248, v214
	v_add_f32_e32 v144, v249, v144
	v_add_f32_e32 v215, v250, v215
	v_add_f32_e32 v145, v251, v145
	v_mul_f32_e32 v170, 0xbfb8aa3b, v170
	v_mul_f32_e32 v142, 0xbfb8aa3b, v142
	v_mul_f32_e32 v171, 0xbfb8aa3b, v171
	v_mul_f32_e32 v143, 0xbfb8aa3b, v143
	v_mul_f32_e32 v214, 0xbfb8aa3b, v214
	v_mul_f32_e32 v144, 0xbfb8aa3b, v144
	v_mul_f32_e32 v215, 0xbfb8aa3b, v215
	v_mul_f32_e32 v145, 0xbfb8aa3b, v145
	v_exp_f32_e32 v170, v170
	v_exp_f32_e32 v142, v142
	v_exp_f32_e32 v171, v171
	v_exp_f32_e32 v143, v143
	v_exp_f32_e32 v214, v214
	v_exp_f32_e32 v144, v144
	v_exp_f32_e32 v215, v215
	v_exp_f32_e32 v145, v145
	v_add_f32_e32 v170, 1.0, v170
	v_add_f32_e32 v142, 1.0, v142
	v_add_f32_e32 v171, 1.0, v171
	v_add_f32_e32 v143, 1.0, v143
	v_add_f32_e32 v214, 1.0, v214
	v_add_f32_e32 v144, 1.0, v144
	v_add_f32_e32 v215, 1.0, v215
	v_add_f32_e32 v145, 1.0, v145
	v_rcp_f32_e32 v170, v170
	v_rcp_f32_e32 v142, v142
	v_rcp_f32_e32 v171, v171
	v_rcp_f32_e32 v143, v143
	v_rcp_f32_e32 v214, v214
	v_rcp_f32_e32 v144, v144
	v_rcp_f32_e32 v215, v215
	v_rcp_f32_e32 v145, v145
	s_waitcnt vmcnt(20)
	v_lshlrev_b32_e32 v221, 16, v240
	v_and_b32_e32 v240, 0xffff0000, v240
	v_lshlrev_b32_e32 v222, 16, v241
	v_and_b32_e32 v241, 0xffff0000, v241
	v_lshlrev_b32_e32 v223, 16, v242
	v_and_b32_e32 v242, 0xffff0000, v242
	v_lshlrev_b32_e32 v224, 16, v243
	v_and_b32_e32 v243, 0xffff0000, v243
	v_fma_f32 v102, v102, v170, v221
	v_fma_f32 v103, v103, v142, v240
	v_fma_f32 v104, v104, v171, v222
	v_fma_f32 v105, v105, v143, v241
	v_fma_f32 v98, v98, v214, v223
	v_fma_f32 v99, v99, v144, v242
	v_fma_f32 v100, v100, v215, v224
	v_fma_f32 v101, v101, v145, v243
	v_cvt_pk_bf16_f32 v102, v102, v103
	v_cvt_pk_bf16_f32 v103, v104, v105
	v_cvt_pk_bf16_f32 v104, v98, v99
	v_cvt_pk_bf16_f32 v105, v100, v101
	v_add_u32_e32 v253, 0xb0000, v226
	global_load_dwordx4 v[240:243], v253, s[4:5]
	v_add_u32_e32 v225, 0x30000, v226
	global_store_dwordx4 v225, v[102:105], s[4:5]
	s_waitcnt vmcnt(21)
	v_lshlrev_b32_e32 v170, 16, v146
	v_and_b32_e32 v146, 0xffff0000, v146
	v_lshlrev_b32_e32 v171, 16, v147
	v_and_b32_e32 v147, 0xffff0000, v147
	v_lshlrev_b32_e32 v214, 16, v148
	v_and_b32_e32 v148, 0xffff0000, v148
	v_lshlrev_b32_e32 v215, 16, v149
	v_and_b32_e32 v149, 0xffff0000, v149
	v_add_f32_e32 v170, v244, v170
	v_add_f32_e32 v146, v245, v146
	v_add_f32_e32 v171, v246, v171
	v_add_f32_e32 v147, v247, v147
	v_add_f32_e32 v214, v248, v214
	v_add_f32_e32 v148, v249, v148
	v_add_f32_e32 v215, v250, v215
	v_add_f32_e32 v149, v251, v149
	v_mul_f32_e32 v170, 0xbfb8aa3b, v170
	v_mul_f32_e32 v146, 0xbfb8aa3b, v146
	v_mul_f32_e32 v171, 0xbfb8aa3b, v171
	v_mul_f32_e32 v147, 0xbfb8aa3b, v147
	v_mul_f32_e32 v214, 0xbfb8aa3b, v214
	v_mul_f32_e32 v148, 0xbfb8aa3b, v148
	v_mul_f32_e32 v215, 0xbfb8aa3b, v215
	v_mul_f32_e32 v149, 0xbfb8aa3b, v149
	v_exp_f32_e32 v170, v170
	v_exp_f32_e32 v146, v146
	v_exp_f32_e32 v171, v171
	v_exp_f32_e32 v147, v147
	v_exp_f32_e32 v214, v214
	v_exp_f32_e32 v148, v148
	v_exp_f32_e32 v215, v215
	v_exp_f32_e32 v149, v149
	v_add_f32_e32 v170, 1.0, v170
	v_add_f32_e32 v146, 1.0, v146
	v_add_f32_e32 v171, 1.0, v171
	v_add_f32_e32 v147, 1.0, v147
	v_add_f32_e32 v214, 1.0, v214
	v_add_f32_e32 v148, 1.0, v148
	v_add_f32_e32 v215, 1.0, v215
	v_add_f32_e32 v149, 1.0, v149
	v_rcp_f32_e32 v170, v170
	v_rcp_f32_e32 v146, v146
	v_rcp_f32_e32 v171, v171
	v_rcp_f32_e32 v147, v147
	v_rcp_f32_e32 v214, v214
	v_rcp_f32_e32 v148, v148
	v_rcp_f32_e32 v215, v215
	v_rcp_f32_e32 v149, v149
	s_waitcnt vmcnt(9)
; __device__ __forceinline__ v4u pack8(const float (&o)[8]) { v4u w; w.x = pk2(o[0], o[1]); w.y = pk2(o[2], o[3]); w.z = pk2(o[4], o[5]); w.w = pk2(o[6], o[7]); return w; }
; __device__ __forceinline__ float sigmf(float x) { return __builtin_amdgcn_rcpf(1.f + __expf(-x)); }
; __device__ __forceinline__ unsigned pk2(float lo, float hi) { typedef float f2v __attribute__((ext_vector_type(2))); typedef __bf16 b2v __attribute__((ext_vector_type(2))); const f2v v = {lo, hi}; return __builtin_bit_cast(unsigned, __builtin_convertvector(v, b2v)); }
; __device__ __forceinline__ void unpack8(const v4u w, float (&o)[8]) { o[0] = bflo(w.x); o[1] = bfhi(w.x); o[2] = bflo(w.y); o[3] = bfhi(w.y); o[4] = bflo(w.z); o[5] = bfhi(w.z); o[6] = bflo(w.w); o[7] = bfhi(w.w); }
;     __device__ __forceinline__ void operator()(const f32x4 (&acc)[2][2][4][2], const pg8::Unit& u, int wr, int wc, int fr, int fq_in) const {
;     ...
;                 for (int m = 0; m < 4; ++m) { const size_t row = (size_t)(row0 + ai * 128 + m * 16);
;                     gw_[m] = *(const v4u*)(Gt + row * (2 * D) + goff + col); pw_[m] = first ? (v4u){0u, 0u, 0u, 0u} : *(const v4u*)(O + row * D + col); }
;                 __builtin_amdgcn_sched_barrier(0);
; #pragma unroll
;                 for (int m = 0; m < 4; ++m) { const size_t row = (size_t)(row0 + ai * 128 + m * 16);
;                     float g0[8], p[8]; unpack8(gw_[m], g0); unpack8(pw_[m], p);
;                     float o[8];
; #pragma unroll
;                     for (int q = 0; q < 4; ++q) { o[q] = p[q] + sigmf(g0[q] + b0[q]) * acc[ai][bj][m][0][q]; o[4 + q] = p[4 + q] + sigmf(g0[4 + q] + b0[4 + q]) * acc[ai][bj][m][1][q]; }
;                     *(v4u*)(O + row * D + col) = pack8(o); }
	v_lshlrev_b32_e32 v221, 16, v228
	v_and_b32_e32 v228, 0xffff0000, v228
	v_lshlrev_b32_e32 v222, 16, v229
	v_and_b32_e32 v229, 0xffff0000, v229
	v_lshlrev_b32_e32 v223, 16, v230
	v_and_b32_e32 v230, 0xffff0000, v230
	v_lshlrev_b32_e32 v224, 16, v231
	v_and_b32_e32 v231, 0xffff0000, v231
	v_fma_f32 v94, v94, v170, v221
	v_fma_f32 v95, v95, v146, v228
	v_fma_f32 v96, v96, v171, v222
	v_fma_f32 v97, v97, v147, v229
	v_fma_f32 v90, v90, v214, v223
	v_fma_f32 v91, v91, v148, v230
	v_fma_f32 v92, v92, v215, v224
	v_fma_f32 v93, v93, v149, v231
	v_cvt_pk_bf16_f32 v94, v94, v95
	v_cvt_pk_bf16_f32 v95, v96, v97
	v_cvt_pk_bf16_f32 v96, v90, v91
	v_cvt_pk_bf16_f32 v97, v92, v93
	global_load_dwordx4 v[228:231], v226, s[4:5] offset:256
	v_add_u32_e32 v225, 0x80000, v226
	global_store_dwordx4 v225, v[94:97], s[4:5]
	s_waitcnt vmcnt(22)
	v_lshlrev_b32_e32 v170, 16, v150
	v_and_b32_e32 v150, 0xffff0000, v150
	v_lshlrev_b32_e32 v171, 16, v151
	v_and_b32_e32 v151, 0xffff0000, v151
	v_lshlrev_b32_e32 v214, 16, v152
	v_and_b32_e32 v152, 0xffff0000, v152
	v_lshlrev_b32_e32 v215, 16, v153
	v_and_b32_e32 v153, 0xffff0000, v153
	v_add_f32_e32 v170, v244, v170
	v_add_f32_e32 v150, v245, v150
	v_add_f32_e32 v171, v246, v171
	v_add_f32_e32 v151, v247, v151
	v_add_f32_e32 v214, v248, v214
	v_add_f32_e32 v152, v249, v152
	v_add_f32_e32 v215, v250, v215
	v_add_f32_e32 v153, v251, v153
	v_mul_f32_e32 v170, 0xbfb8aa3b, v170
	v_mul_f32_e32 v150, 0xbfb8aa3b, v150
	v_mul_f32_e32 v171, 0xbfb8aa3b, v171
	v_mul_f32_e32 v151, 0xbfb8aa3b, v151
	v_mul_f32_e32 v214, 0xbfb8aa3b, v214
	v_mul_f32_e32 v152, 0xbfb8aa3b, v152
	v_mul_f32_e32 v215, 0xbfb8aa3b, v215
	v_mul_f32_e32 v153, 0xbfb8aa3b, v153
	v_exp_f32_e32 v170, v170
	v_exp_f32_e32 v150, v150
	v_exp_f32_e32 v171, v171
	v_exp_f32_e32 v151, v151
	v_exp_f32_e32 v214, v214
	v_exp_f32_e32 v152, v152
	v_exp_f32_e32 v215, v215
	v_exp_f32_e32 v153, v153
	v_add_f32_e32 v170, 1.0, v170
	v_add_f32_e32 v150, 1.0, v150
	v_add_f32_e32 v171, 1.0, v171
	v_add_f32_e32 v151, 1.0, v151
	v_add_f32_e32 v214, 1.0, v214
	v_add_f32_e32 v152, 1.0, v152
	v_add_f32_e32 v215, 1.0, v215
	v_add_f32_e32 v153, 1.0, v153
	v_rcp_f32_e32 v170, v170
	v_rcp_f32_e32 v150, v150
	v_rcp_f32_e32 v171, v171
	v_rcp_f32_e32 v151, v151
	v_rcp_f32_e32 v214, v214
	v_rcp_f32_e32 v152, v152
	v_rcp_f32_e32 v215, v215
	v_rcp_f32_e32 v153, v153
	s_waitcnt vmcnt(9)
	v_lshlrev_b32_e32 v221, 16, v232
	v_and_b32_e32 v232, 0xffff0000, v232
	v_lshlrev_b32_e32 v222, 16, v233
	v_and_b32_e32 v233, 0xffff0000, v233
	v_lshlrev_b32_e32 v223, 16, v234
	v_and_b32_e32 v234, 0xffff0000, v234
	v_lshlrev_b32_e32 v224, 16, v235
	v_and_b32_e32 v235, 0xffff0000, v235
	v_fma_f32 v86, v86, v170, v221
	v_fma_f32 v87, v87, v150, v232
	v_fma_f32 v88, v88, v171, v222
	v_fma_f32 v89, v89, v151, v233
	v_fma_f32 v82, v82, v214, v223
	v_fma_f32 v83, v83, v152, v234
	v_fma_f32 v84, v84, v215, v224
	v_fma_f32 v85, v85, v153, v235
	v_cvt_pk_bf16_f32 v86, v86, v87
	v_cvt_pk_bf16_f32 v87, v88, v89
	v_cvt_pk_bf16_f32 v88, v82, v83
	v_cvt_pk_bf16_f32 v89, v84, v85
	v_add_u32_e32 v253, 0x10000, v226
	global_load_dwordx4 v[232:235], v253, s[4:5] offset:256
	v_add_u32_e32 v225, 0x90000, v226
	global_store_dwordx4 v225, v[86:89], s[4:5]
	s_waitcnt vmcnt(23)
	v_lshlrev_b32_e32 v170, 16, v154
	v_and_b32_e32 v154, 0xffff0000, v154
	v_lshlrev_b32_e32 v171, 16, v155
	v_and_b32_e32 v155, 0xffff0000, v155
	v_lshlrev_b32_e32 v214, 16, v156
	v_and_b32_e32 v156, 0xffff0000, v156
	v_lshlrev_b32_e32 v215, 16, v157
	v_and_b32_e32 v157, 0xffff0000, v157
	v_add_f32_e32 v170, v244, v170
	v_add_f32_e32 v154, v245, v154
	v_add_f32_e32 v171, v246, v171
	v_add_f32_e32 v155, v247, v155
	v_add_f32_e32 v214, v248, v214
	v_add_f32_e32 v156, v249, v156
	v_add_f32_e32 v215, v250, v215
	v_add_f32_e32 v157, v251, v157
	v_mul_f32_e32 v170, 0xbfb8aa3b, v170
	v_mul_f32_e32 v154, 0xbfb8aa3b, v154
	v_mul_f32_e32 v171, 0xbfb8aa3b, v171
	v_mul_f32_e32 v155, 0xbfb8aa3b, v155
	v_mul_f32_e32 v214, 0xbfb8aa3b, v214
	v_mul_f32_e32 v156, 0xbfb8aa3b, v156
	v_mul_f32_e32 v215, 0xbfb8aa3b, v215
	v_mul_f32_e32 v157, 0xbfb8aa3b, v157
	v_exp_f32_e32 v170, v170
	v_exp_f32_e32 v154, v154
	v_exp_f32_e32 v171, v171
	v_exp_f32_e32 v155, v155
	v_exp_f32_e32 v214, v214
	v_exp_f32_e32 v156, v156
	v_exp_f32_e32 v215, v215
	v_exp_f32_e32 v157, v157
	v_add_f32_e32 v170, 1.0, v170
	v_add_f32_e32 v154, 1.0, v154
	v_add_f32_e32 v171, 1.0, v171
	v_add_f32_e32 v155, 1.0, v155
	v_add_f32_e32 v214, 1.0, v214
	v_add_f32_e32 v156, 1.0, v156
	v_add_f32_e32 v215, 1.0, v215
	v_add_f32_e32 v157, 1.0, v157
	v_rcp_f32_e32 v170, v170
	v_rcp_f32_e32 v154, v154
	v_rcp_f32_e32 v171, v171
	v_rcp_f32_e32 v155, v155
	v_rcp_f32_e32 v214, v214
	v_rcp_f32_e32 v156, v156
	v_rcp_f32_e32 v215, v215
	v_rcp_f32_e32 v157, v157
	s_waitcnt vmcnt(7)
	v_lshlrev_b32_e32 v221, 16, v236
	v_and_b32_e32 v236, 0xffff0000, v236
	v_lshlrev_b32_e32 v222, 16, v237
	v_and_b32_e32 v237, 0xffff0000, v237
	v_lshlrev_b32_e32 v223, 16, v238
	v_and_b32_e32 v238, 0xffff0000, v238
	v_lshlrev_b32_e32 v224, 16, v239
	v_and_b32_e32 v239, 0xffff0000, v239
	v_fma_f32 v78, v78, v170, v221
	v_fma_f32 v79, v79, v154, v236
	v_fma_f32 v80, v80, v171, v222
	v_fma_f32 v81, v81, v155, v237
	v_fma_f32 v74, v74, v214, v223
	v_fma_f32 v75, v75, v156, v238
	v_fma_f32 v76, v76, v215, v224
	v_fma_f32 v77, v77, v157, v239
	v_cvt_pk_bf16_f32 v78, v78, v79
	v_cvt_pk_bf16_f32 v79, v80, v81
	v_cvt_pk_bf16_f32 v80, v74, v75
	v_cvt_pk_bf16_f32 v81, v76, v77
	v_add_u32_e32 v253, 0x20000, v226
	global_load_dwordx4 v[236:239], v253, s[4:5] offset:256
	v_add_u32_e32 v225, 0xa0000, v226
	global_store_dwordx4 v225, v[78:81], s[4:5]
	s_waitcnt vmcnt(24)
; __device__ __forceinline__ v4u pack8(const float (&o)[8]) { v4u w; w.x = pk2(o[0], o[1]); w.y = pk2(o[2], o[3]); w.z = pk2(o[4], o[5]); w.w = pk2(o[6], o[7]); return w; }
; __device__ __forceinline__ float sigmf(float x) { return __builtin_amdgcn_rcpf(1.f + __expf(-x)); }
; __device__ __forceinline__ unsigned pk2(float lo, float hi) { typedef float f2v __attribute__((ext_vector_type(2))); typedef __bf16 b2v __attribute__((ext_vector_type(2))); const f2v v = {lo, hi}; return __builtin_bit_cast(unsigned, __builtin_convertvector(v, b2v)); }
; __device__ __forceinline__ void unpack8(const v4u w, float (&o)[8]) { o[0] = bflo(w.x); o[1] = bfhi(w.x); o[2] = bflo(w.y); o[3] = bfhi(w.y); o[4] = bflo(w.z); o[5] = bfhi(w.z); o[6] = bflo(w.w); o[7] = bfhi(w.w); }
;     __device__ __forceinline__ void operator()(const f32x4 (&acc)[2][2][4][2], const pg8::Unit& u, int wr, int wc, int fr, int fq_in) const {
;     ...
;                 for (int m = 0; m < 4; ++m) { const size_t row = (size_t)(row0 + ai * 128 + m * 16);
;                     gw_[m] = *(const v4u*)(Gt + row * (2 * D) + goff + col); pw_[m] = first ? (v4u){0u, 0u, 0u, 0u} : *(const v4u*)(O + row * D + col); }
;                 __builtin_amdgcn_sched_barrier(0);
; #pragma unroll
;                 for (int m = 0; m < 4; ++m) { const size_t row = (size_t)(row0 + ai * 128 + m * 16);
;                     float g0[8], p[8]; unpack8(gw_[m], g0); unpack8(pw_[m], p);
;                     float o[8];
; #pragma unroll
;                     for (int q = 0; q < 4; ++q) { o[q] = p[q] + sigmf(g0[q] + b0[q]) * acc[ai][bj][m][0][q]; o[4 + q] = p[4 + q] + sigmf(g0[4 + q] + b0[4 + q]) * acc[ai][bj][m][1][q]; }
;                     *(v4u*)(O + row * D + col) = pack8(o); }
	v_lshlrev_b32_e32 v170, 16, v158
	v_and_b32_e32 v158, 0xffff0000, v158
	v_lshlrev_b32_e32 v171, 16, v159
	v_and_b32_e32 v159, 0xffff0000, v159
	v_lshlrev_b32_e32 v214, 16, v160
	v_and_b32_e32 v160, 0xffff0000, v160
	v_lshlrev_b32_e32 v215, 16, v161
	v_and_b32_e32 v161, 0xffff0000, v161
	v_add_f32_e32 v170, v244, v170
	v_add_f32_e32 v158, v245, v158
	v_add_f32_e32 v171, v246, v171
	v_add_f32_e32 v159, v247, v159
	v_add_f32_e32 v214, v248, v214
	v_add_f32_e32 v160, v249, v160
	v_add_f32_e32 v215, v250, v215
	v_add_f32_e32 v161, v251, v161
	v_mul_f32_e32 v170, 0xbfb8aa3b, v170
	v_mul_f32_e32 v158, 0xbfb8aa3b, v158
	v_mul_f32_e32 v171, 0xbfb8aa3b, v171
	v_mul_f32_e32 v159, 0xbfb8aa3b, v159
	v_mul_f32_e32 v214, 0xbfb8aa3b, v214
	v_mul_f32_e32 v160, 0xbfb8aa3b, v160
	v_mul_f32_e32 v215, 0xbfb8aa3b, v215
	v_mul_f32_e32 v161, 0xbfb8aa3b, v161
	v_exp_f32_e32 v170, v170
	v_exp_f32_e32 v158, v158
	v_exp_f32_e32 v171, v171
	v_exp_f32_e32 v159, v159
	v_exp_f32_e32 v214, v214
	v_exp_f32_e32 v160, v160
	v_exp_f32_e32 v215, v215
	v_exp_f32_e32 v161, v161
	v_add_f32_e32 v170, 1.0, v170
	v_add_f32_e32 v158, 1.0, v158
	v_add_f32_e32 v171, 1.0, v171
	v_add_f32_e32 v159, 1.0, v159
	v_add_f32_e32 v214, 1.0, v214
	v_add_f32_e32 v160, 1.0, v160
	v_add_f32_e32 v215, 1.0, v215
	v_add_f32_e32 v161, 1.0, v161
	v_rcp_f32_e32 v170, v170
	v_rcp_f32_e32 v158, v158
	v_rcp_f32_e32 v171, v171
	v_rcp_f32_e32 v159, v159
	v_rcp_f32_e32 v214, v214
	v_rcp_f32_e32 v160, v160
	v_rcp_f32_e32 v215, v215
	v_rcp_f32_e32 v161, v161
	s_waitcnt vmcnt(7)
	v_lshlrev_b32_e32 v221, 16, v240
	v_and_b32_e32 v240, 0xffff0000, v240
	v_lshlrev_b32_e32 v222, 16, v241
	v_and_b32_e32 v241, 0xffff0000, v241
	v_lshlrev_b32_e32 v223, 16, v242
	v_and_b32_e32 v242, 0xffff0000, v242
	v_lshlrev_b32_e32 v224, 16, v243
	v_and_b32_e32 v243, 0xffff0000, v243
	v_fma_f32 v70, v70, v170, v221
	v_fma_f32 v71, v71, v158, v240
	v_fma_f32 v72, v72, v171, v222
	v_fma_f32 v73, v73, v159, v241
	v_fma_f32 v66, v66, v214, v223
	v_fma_f32 v67, v67, v160, v242
	v_fma_f32 v68, v68, v215, v224
	v_fma_f32 v69, v69, v161, v243
	v_cvt_pk_bf16_f32 v70, v70, v71
	v_cvt_pk_bf16_f32 v71, v72, v73
	v_cvt_pk_bf16_f32 v72, v66, v67
	v_cvt_pk_bf16_f32 v73, v68, v69
	v_add_u32_e32 v253, 0x30000, v226
	global_load_dwordx4 v[240:243], v253, s[4:5] offset:256
	v_add_u32_e32 v225, 0xb0000, v226
	global_store_dwordx4 v225, v[70:73], s[4:5]
	s_waitcnt vmcnt(12)
	s_waitcnt vmcnt(25)
	v_lshlrev_b32_e32 v170, 16, v162
	v_and_b32_e32 v162, 0xffff0000, v162
	v_lshlrev_b32_e32 v171, 16, v163
	v_and_b32_e32 v163, 0xffff0000, v163
	v_lshlrev_b32_e32 v214, 16, v164
	v_and_b32_e32 v164, 0xffff0000, v164
	v_lshlrev_b32_e32 v215, 16, v165
	v_and_b32_e32 v165, 0xffff0000, v165
	v_add_f32_e32 v170, v130, v170
	v_add_f32_e32 v162, v131, v162
	v_add_f32_e32 v171, v132, v171
	v_add_f32_e32 v163, v133, v163
	v_add_f32_e32 v214, v122, v214
	v_add_f32_e32 v164, v123, v164
	v_add_f32_e32 v215, v124, v215
	v_add_f32_e32 v165, v125, v165
	v_mul_f32_e32 v170, 0xbfb8aa3b, v170
	v_mul_f32_e32 v162, 0xbfb8aa3b, v162
	v_mul_f32_e32 v171, 0xbfb8aa3b, v171
	v_mul_f32_e32 v163, 0xbfb8aa3b, v163
	v_mul_f32_e32 v214, 0xbfb8aa3b, v214
	v_mul_f32_e32 v164, 0xbfb8aa3b, v164
	v_mul_f32_e32 v215, 0xbfb8aa3b, v215
	v_mul_f32_e32 v165, 0xbfb8aa3b, v165
	v_exp_f32_e32 v170, v170
	v_exp_f32_e32 v162, v162
	v_exp_f32_e32 v171, v171
	v_exp_f32_e32 v163, v163
	v_exp_f32_e32 v214, v214
	v_exp_f32_e32 v164, v164
	v_exp_f32_e32 v215, v215
	v_exp_f32_e32 v165, v165
	v_add_f32_e32 v170, 1.0, v170
	v_add_f32_e32 v162, 1.0, v162
	v_add_f32_e32 v171, 1.0, v171
	v_add_f32_e32 v163, 1.0, v163
	v_add_f32_e32 v214, 1.0, v214
	v_add_f32_e32 v164, 1.0, v164
	v_add_f32_e32 v215, 1.0, v215
	v_add_f32_e32 v165, 1.0, v165
	v_rcp_f32_e32 v170, v170
	v_rcp_f32_e32 v162, v162
	v_rcp_f32_e32 v171, v171
	v_rcp_f32_e32 v163, v163
	v_rcp_f32_e32 v214, v214
	v_rcp_f32_e32 v164, v164
	v_rcp_f32_e32 v215, v215
	v_rcp_f32_e32 v165, v165
	s_waitcnt vmcnt(7)
	v_lshlrev_b32_e32 v221, 16, v228
	v_and_b32_e32 v228, 0xffff0000, v228
	v_lshlrev_b32_e32 v222, 16, v229
	v_and_b32_e32 v229, 0xffff0000, v229
	v_lshlrev_b32_e32 v223, 16, v230
	v_and_b32_e32 v230, 0xffff0000, v230
	v_lshlrev_b32_e32 v224, 16, v231
	v_and_b32_e32 v231, 0xffff0000, v231
	v_fma_f32 v62, v62, v170, v221
	v_fma_f32 v63, v63, v162, v228
	v_fma_f32 v64, v64, v171, v222
	v_fma_f32 v65, v65, v163, v229
	v_fma_f32 v58, v58, v214, v223
	v_fma_f32 v59, v59, v164, v230
	v_fma_f32 v60, v60, v215, v224
	v_fma_f32 v61, v61, v165, v231
	v_cvt_pk_bf16_f32 v62, v62, v63
	v_cvt_pk_bf16_f32 v63, v64, v65
	v_cvt_pk_bf16_f32 v64, v58, v59
	v_cvt_pk_bf16_f32 v65, v60, v61
	v_add_u32_e32 v253, 0x80000, v226
	global_load_dwordx4 v[228:231], v253, s[4:5] offset:256
	global_store_dwordx4 v226, v[62:65], s[4:5] offset:256
	s_waitcnt vmcnt(26)
	v_lshlrev_b32_e32 v170, 16, v166
	v_and_b32_e32 v166, 0xffff0000, v166
	v_lshlrev_b32_e32 v171, 16, v167
	v_and_b32_e32 v167, 0xffff0000, v167
	v_lshlrev_b32_e32 v214, 16, v168
	v_and_b32_e32 v168, 0xffff0000, v168
	v_lshlrev_b32_e32 v215, 16, v169
	v_and_b32_e32 v169, 0xffff0000, v169
	v_add_f32_e32 v170, v130, v170
	v_add_f32_e32 v166, v131, v166
	v_add_f32_e32 v171, v132, v171
	v_add_f32_e32 v167, v133, v167
	v_add_f32_e32 v214, v122, v214
	v_add_f32_e32 v168, v123, v168
	v_add_f32_e32 v215, v124, v215
	v_add_f32_e32 v169, v125, v169
	v_mul_f32_e32 v170, 0xbfb8aa3b, v170
	v_mul_f32_e32 v166, 0xbfb8aa3b, v166
	v_mul_f32_e32 v171, 0xbfb8aa3b, v171
	v_mul_f32_e32 v167, 0xbfb8aa3b, v167
	v_mul_f32_e32 v214, 0xbfb8aa3b, v214
	v_mul_f32_e32 v168, 0xbfb8aa3b, v168
	v_mul_f32_e32 v215, 0xbfb8aa3b, v215
	v_mul_f32_e32 v169, 0xbfb8aa3b, v169
	v_exp_f32_e32 v170, v170
	v_exp_f32_e32 v166, v166
	v_exp_f32_e32 v171, v171
	v_exp_f32_e32 v167, v167
	v_exp_f32_e32 v214, v214
	v_exp_f32_e32 v168, v168
	v_exp_f32_e32 v215, v215
	v_exp_f32_e32 v169, v169
	v_add_f32_e32 v170, 1.0, v170
	v_add_f32_e32 v166, 1.0, v166
	v_add_f32_e32 v171, 1.0, v171
	v_add_f32_e32 v167, 1.0, v167
	v_add_f32_e32 v214, 1.0, v214
	v_add_f32_e32 v168, 1.0, v168
	v_add_f32_e32 v215, 1.0, v215
	v_add_f32_e32 v169, 1.0, v169
	v_rcp_f32_e32 v170, v170
	v_rcp_f32_e32 v166, v166
	v_rcp_f32_e32 v171, v171
	v_rcp_f32_e32 v167, v167
	v_rcp_f32_e32 v214, v214
	v_rcp_f32_e32 v168, v168
	v_rcp_f32_e32 v215, v215
	v_rcp_f32_e32 v169, v169
	s_waitcnt vmcnt(7)
; __device__ __forceinline__ v4u pack8(const float (&o)[8]) { v4u w; w.x = pk2(o[0], o[1]); w.y = pk2(o[2], o[3]); w.z = pk2(o[4], o[5]); w.w = pk2(o[6], o[7]); return w; }
; __device__ __forceinline__ float sigmf(float x) { return __builtin_amdgcn_rcpf(1.f + __expf(-x)); }
; __device__ __forceinline__ unsigned pk2(float lo, float hi) { typedef float f2v __attribute__((ext_vector_type(2))); typedef __bf16 b2v __attribute__((ext_vector_type(2))); const f2v v = {lo, hi}; return __builtin_bit_cast(unsigned, __builtin_convertvector(v, b2v)); }
; __device__ __forceinline__ void unpack8(const v4u w, float (&o)[8]) { o[0] = bflo(w.x); o[1] = bfhi(w.x); o[2] = bflo(w.y); o[3] = bfhi(w.y); o[4] = bflo(w.z); o[5] = bfhi(w.z); o[6] = bflo(w.w); o[7] = bfhi(w.w); }
;     __device__ __forceinline__ void operator()(const f32x4 (&acc)[2][2][4][2], const pg8::Unit& u, int wr, int wc, int fr, int fq_in) const {
;     ...
;                 for (int m = 0; m < 4; ++m) { const size_t row = (size_t)(row0 + ai * 128 + m * 16);
;                     gw_[m] = *(const v4u*)(Gt + row * (2 * D) + goff + col); pw_[m] = first ? (v4u){0u, 0u, 0u, 0u} : *(const v4u*)(O + row * D + col); }
;                 __builtin_amdgcn_sched_barrier(0);
; #pragma unroll
;                 for (int m = 0; m < 4; ++m) { const size_t row = (size_t)(row0 + ai * 128 + m * 16);
;                     float g0[8], p[8]; unpack8(gw_[m], g0); unpack8(pw_[m], p);
;                     float o[8];
; #pragma unroll
;                     for (int q = 0; q < 4; ++q) { o[q] = p[q] + sigmf(g0[q] + b0[q]) * acc[ai][bj][m][0][q]; o[4 + q] = p[4 + q] + sigmf(g0[4 + q] + b0[4 + q]) * acc[ai][bj][m][1][q]; }
;                     *(v4u*)(O + row * D + col) = pack8(o); }
	v_lshlrev_b32_e32 v221, 16, v232
	v_and_b32_e32 v232, 0xffff0000, v232
	v_lshlrev_b32_e32 v222, 16, v233
	v_and_b32_e32 v233, 0xffff0000, v233
	v_lshlrev_b32_e32 v223, 16, v234
	v_and_b32_e32 v234, 0xffff0000, v234
	v_lshlrev_b32_e32 v224, 16, v235
	v_and_b32_e32 v235, 0xffff0000, v235
	v_fma_f32 v54, v54, v170, v221
	v_fma_f32 v55, v55, v166, v232
	v_fma_f32 v56, v56, v171, v222
	v_fma_f32 v57, v57, v167, v233
	v_fma_f32 v50, v50, v214, v223
	v_fma_f32 v51, v51, v168, v234
	v_fma_f32 v52, v52, v215, v224
	v_fma_f32 v53, v53, v169, v235
	v_cvt_pk_bf16_f32 v54, v54, v55
	v_cvt_pk_bf16_f32 v55, v56, v57
	v_cvt_pk_bf16_f32 v56, v50, v51
	v_cvt_pk_bf16_f32 v57, v52, v53
	v_add_u32_e32 v253, 0x90000, v226
	global_load_dwordx4 v[232:235], v253, s[4:5] offset:256
	v_add_u32_e32 v225, 0x10000, v226
	global_store_dwordx4 v225, v[54:57], s[4:5] offset:256
	s_waitcnt vmcnt(27)
	v_lshlrev_b32_e32 v170, 16, v190
	v_and_b32_e32 v190, 0xffff0000, v190
	v_lshlrev_b32_e32 v171, 16, v191
	v_and_b32_e32 v191, 0xffff0000, v191
	v_lshlrev_b32_e32 v214, 16, v192
	v_and_b32_e32 v192, 0xffff0000, v192
	v_lshlrev_b32_e32 v215, 16, v193
	v_and_b32_e32 v193, 0xffff0000, v193
	v_add_f32_e32 v170, v130, v170
	v_add_f32_e32 v190, v131, v190
	v_add_f32_e32 v171, v132, v171
	v_add_f32_e32 v191, v133, v191
	v_add_f32_e32 v214, v122, v214
	v_add_f32_e32 v192, v123, v192
	v_add_f32_e32 v215, v124, v215
	v_add_f32_e32 v193, v125, v193
	v_mul_f32_e32 v170, 0xbfb8aa3b, v170
	v_mul_f32_e32 v190, 0xbfb8aa3b, v190
	v_mul_f32_e32 v171, 0xbfb8aa3b, v171
	v_mul_f32_e32 v191, 0xbfb8aa3b, v191
	v_mul_f32_e32 v214, 0xbfb8aa3b, v214
	v_mul_f32_e32 v192, 0xbfb8aa3b, v192
	v_mul_f32_e32 v215, 0xbfb8aa3b, v215
	v_mul_f32_e32 v193, 0xbfb8aa3b, v193
	v_exp_f32_e32 v170, v170
	v_exp_f32_e32 v190, v190
	v_exp_f32_e32 v171, v171
	v_exp_f32_e32 v191, v191
	v_exp_f32_e32 v214, v214
	v_exp_f32_e32 v192, v192
	v_exp_f32_e32 v215, v215
	v_exp_f32_e32 v193, v193
	v_add_f32_e32 v170, 1.0, v170
	v_add_f32_e32 v190, 1.0, v190
	v_add_f32_e32 v171, 1.0, v171
	v_add_f32_e32 v191, 1.0, v191
	v_add_f32_e32 v214, 1.0, v214
	v_add_f32_e32 v192, 1.0, v192
	v_add_f32_e32 v215, 1.0, v215
	v_add_f32_e32 v193, 1.0, v193
	v_rcp_f32_e32 v170, v170
	v_rcp_f32_e32 v190, v190
	v_rcp_f32_e32 v171, v171
	v_rcp_f32_e32 v191, v191
	v_rcp_f32_e32 v214, v214
	v_rcp_f32_e32 v192, v192
	v_rcp_f32_e32 v215, v215
	v_rcp_f32_e32 v193, v193
	s_waitcnt vmcnt(7)
	v_lshlrev_b32_e32 v221, 16, v236
	v_and_b32_e32 v236, 0xffff0000, v236
	v_lshlrev_b32_e32 v222, 16, v237
	v_and_b32_e32 v237, 0xffff0000, v237
	v_lshlrev_b32_e32 v223, 16, v238
	v_and_b32_e32 v238, 0xffff0000, v238
	v_lshlrev_b32_e32 v224, 16, v239
	v_and_b32_e32 v239, 0xffff0000, v239
	v_fma_f32 v46, v46, v170, v221
	v_fma_f32 v47, v47, v190, v236
	v_fma_f32 v48, v48, v171, v222
	v_fma_f32 v49, v49, v191, v237
	v_fma_f32 v42, v42, v214, v223
	v_fma_f32 v43, v43, v192, v238
	v_fma_f32 v44, v44, v215, v224
	v_fma_f32 v45, v45, v193, v239
	v_cvt_pk_bf16_f32 v46, v46, v47
	v_cvt_pk_bf16_f32 v47, v48, v49
	v_cvt_pk_bf16_f32 v48, v42, v43
	v_cvt_pk_bf16_f32 v49, v44, v45
	v_add_u32_e32 v253, 0xa0000, v226
	global_load_dwordx4 v[236:239], v253, s[4:5] offset:256
	v_add_u32_e32 v225, 0x20000, v226
	global_store_dwordx4 v225, v[46:49], s[4:5] offset:256
	s_waitcnt vmcnt(28)
	v_lshlrev_b32_e32 v170, 16, v194
	v_and_b32_e32 v194, 0xffff0000, v194
	v_lshlrev_b32_e32 v171, 16, v195
	v_and_b32_e32 v195, 0xffff0000, v195
	v_lshlrev_b32_e32 v214, 16, v196
	v_and_b32_e32 v196, 0xffff0000, v196
	v_lshlrev_b32_e32 v215, 16, v197
	v_and_b32_e32 v197, 0xffff0000, v197
	v_add_f32_e32 v170, v130, v170
	v_add_f32_e32 v194, v131, v194
	v_add_f32_e32 v171, v132, v171
	v_add_f32_e32 v195, v133, v195
	v_add_f32_e32 v214, v122, v214
	v_add_f32_e32 v196, v123, v196
	v_add_f32_e32 v215, v124, v215
	v_add_f32_e32 v197, v125, v197
	v_mul_f32_e32 v170, 0xbfb8aa3b, v170
	v_mul_f32_e32 v194, 0xbfb8aa3b, v194
	v_mul_f32_e32 v171, 0xbfb8aa3b, v171
	v_mul_f32_e32 v195, 0xbfb8aa3b, v195
	v_mul_f32_e32 v214, 0xbfb8aa3b, v214
	v_mul_f32_e32 v196, 0xbfb8aa3b, v196
	v_mul_f32_e32 v215, 0xbfb8aa3b, v215
	v_mul_f32_e32 v197, 0xbfb8aa3b, v197
	v_exp_f32_e32 v170, v170
	v_exp_f32_e32 v194, v194
	v_exp_f32_e32 v171, v171
	v_exp_f32_e32 v195, v195
	v_exp_f32_e32 v214, v214
	v_exp_f32_e32 v196, v196
	v_exp_f32_e32 v215, v215
	v_exp_f32_e32 v197, v197
	v_add_f32_e32 v170, 1.0, v170
	v_add_f32_e32 v194, 1.0, v194
	v_add_f32_e32 v171, 1.0, v171
	v_add_f32_e32 v195, 1.0, v195
	v_add_f32_e32 v214, 1.0, v214
	v_add_f32_e32 v196, 1.0, v196
	v_add_f32_e32 v215, 1.0, v215
	v_add_f32_e32 v197, 1.0, v197
	v_rcp_f32_e32 v170, v170
	v_rcp_f32_e32 v194, v194
	v_rcp_f32_e32 v171, v171
	v_rcp_f32_e32 v195, v195
	v_rcp_f32_e32 v214, v214
	v_rcp_f32_e32 v196, v196
	v_rcp_f32_e32 v215, v215
	v_rcp_f32_e32 v197, v197
	s_waitcnt vmcnt(7)
	v_lshlrev_b32_e32 v221, 16, v240
	v_and_b32_e32 v240, 0xffff0000, v240
	v_lshlrev_b32_e32 v222, 16, v241
	v_and_b32_e32 v241, 0xffff0000, v241
	v_lshlrev_b32_e32 v223, 16, v242
	v_and_b32_e32 v242, 0xffff0000, v242
	v_lshlrev_b32_e32 v224, 16, v243
	v_and_b32_e32 v243, 0xffff0000, v243
	v_fma_f32 v38, v38, v170, v221
	v_fma_f32 v39, v39, v194, v240
	v_fma_f32 v40, v40, v171, v222
	v_fma_f32 v41, v41, v195, v241
	v_fma_f32 v34, v34, v214, v223
	v_fma_f32 v35, v35, v196, v242
	v_fma_f32 v36, v36, v215, v224
	v_fma_f32 v37, v37, v197, v243
	v_cvt_pk_bf16_f32 v38, v38, v39
	v_cvt_pk_bf16_f32 v39, v40, v41
	v_cvt_pk_bf16_f32 v40, v34, v35
	v_cvt_pk_bf16_f32 v41, v36, v37
	v_add_u32_e32 v253, 0xb0000, v226
	global_load_dwordx4 v[240:243], v253, s[4:5] offset:256
	v_add_u32_e32 v225, 0x30000, v226
	global_store_dwordx4 v225, v[38:41], s[4:5] offset:256
	s_waitcnt vmcnt(29)
; __device__ __forceinline__ v4u pack8(const float (&o)[8]) { v4u w; w.x = pk2(o[0], o[1]); w.y = pk2(o[2], o[3]); w.z = pk2(o[4], o[5]); w.w = pk2(o[6], o[7]); return w; }
; __device__ __forceinline__ float sigmf(float x) { return __builtin_amdgcn_rcpf(1.f + __expf(-x)); }
; __device__ __forceinline__ unsigned pk2(float lo, float hi) { typedef float f2v __attribute__((ext_vector_type(2))); typedef __bf16 b2v __attribute__((ext_vector_type(2))); const f2v v = {lo, hi}; return __builtin_bit_cast(unsigned, __builtin_convertvector(v, b2v)); }
; __device__ __forceinline__ void unpack8(const v4u w, float (&o)[8]) { o[0] = bflo(w.x); o[1] = bfhi(w.x); o[2] = bflo(w.y); o[3] = bfhi(w.y); o[4] = bflo(w.z); o[5] = bfhi(w.z); o[6] = bflo(w.w); o[7] = bfhi(w.w); }
;     __device__ __forceinline__ void operator()(const f32x4 (&acc)[2][2][4][2], const pg8::Unit& u, int wr, int wc, int fr, int fq_in) const {
;     ...
;                 for (int m = 0; m < 4; ++m) { const size_t row = (size_t)(row0 + ai * 128 + m * 16);
;                     gw_[m] = *(const v4u*)(Gt + row * (2 * D) + goff + col); pw_[m] = first ? (v4u){0u, 0u, 0u, 0u} : *(const v4u*)(O + row * D + col); }
;                 __builtin_amdgcn_sched_barrier(0);
; #pragma unroll
;                 for (int m = 0; m < 4; ++m) { const size_t row = (size_t)(row0 + ai * 128 + m * 16);
;                     float g0[8], p[8]; unpack8(gw_[m], g0); unpack8(pw_[m], p);
;                     float o[8];
; #pragma unroll
;                     for (int q = 0; q < 4; ++q) { o[q] = p[q] + sigmf(g0[q] + b0[q]) * acc[ai][bj][m][0][q]; o[4 + q] = p[4 + q] + sigmf(g0[4 + q] + b0[4 + q]) * acc[ai][bj][m][1][q]; }
;                     *(v4u*)(O + row * D + col) = pack8(o); }
	v_lshlrev_b32_e32 v170, 16, v198
	v_and_b32_e32 v198, 0xffff0000, v198
	v_lshlrev_b32_e32 v171, 16, v199
	v_and_b32_e32 v199, 0xffff0000, v199
	v_lshlrev_b32_e32 v214, 16, v200
	v_and_b32_e32 v200, 0xffff0000, v200
	v_lshlrev_b32_e32 v215, 16, v201
	v_and_b32_e32 v201, 0xffff0000, v201
	v_add_f32_e32 v170, v130, v170
	v_add_f32_e32 v198, v131, v198
	v_add_f32_e32 v171, v132, v171
	v_add_f32_e32 v199, v133, v199
	v_add_f32_e32 v214, v122, v214
	v_add_f32_e32 v200, v123, v200
	v_add_f32_e32 v215, v124, v215
	v_add_f32_e32 v201, v125, v201
	v_mul_f32_e32 v170, 0xbfb8aa3b, v170
	v_mul_f32_e32 v198, 0xbfb8aa3b, v198
	v_mul_f32_e32 v171, 0xbfb8aa3b, v171
	v_mul_f32_e32 v199, 0xbfb8aa3b, v199
	v_mul_f32_e32 v214, 0xbfb8aa3b, v214
	v_mul_f32_e32 v200, 0xbfb8aa3b, v200
	v_mul_f32_e32 v215, 0xbfb8aa3b, v215
	v_mul_f32_e32 v201, 0xbfb8aa3b, v201
	v_exp_f32_e32 v170, v170
	v_exp_f32_e32 v198, v198
	v_exp_f32_e32 v171, v171
	v_exp_f32_e32 v199, v199
	v_exp_f32_e32 v214, v214
	v_exp_f32_e32 v200, v200
	v_exp_f32_e32 v215, v215
	v_exp_f32_e32 v201, v201
	v_add_f32_e32 v170, 1.0, v170
	v_add_f32_e32 v198, 1.0, v198
	v_add_f32_e32 v171, 1.0, v171
	v_add_f32_e32 v199, 1.0, v199
	v_add_f32_e32 v214, 1.0, v214
	v_add_f32_e32 v200, 1.0, v200
	v_add_f32_e32 v215, 1.0, v215
	v_add_f32_e32 v201, 1.0, v201
	v_rcp_f32_e32 v170, v170
	v_rcp_f32_e32 v198, v198
	v_rcp_f32_e32 v171, v171
	v_rcp_f32_e32 v199, v199
	v_rcp_f32_e32 v214, v214
	v_rcp_f32_e32 v200, v200
	v_rcp_f32_e32 v215, v215
	v_rcp_f32_e32 v201, v201
	s_waitcnt vmcnt(7)
	v_lshlrev_b32_e32 v221, 16, v228
	v_and_b32_e32 v228, 0xffff0000, v228
	v_lshlrev_b32_e32 v222, 16, v229
	v_and_b32_e32 v229, 0xffff0000, v229
	v_lshlrev_b32_e32 v223, 16, v230
	v_and_b32_e32 v230, 0xffff0000, v230
	v_lshlrev_b32_e32 v224, 16, v231
	v_and_b32_e32 v231, 0xffff0000, v231
	v_fma_f32 v30, v30, v170, v221
	v_fma_f32 v31, v31, v198, v228
	v_fma_f32 v32, v32, v171, v222
	v_fma_f32 v33, v33, v199, v229
	v_fma_f32 v26, v26, v214, v223
	v_fma_f32 v27, v27, v200, v230
	v_fma_f32 v28, v28, v215, v224
	v_fma_f32 v29, v29, v201, v231
	v_cvt_pk_bf16_f32 v30, v30, v31
	v_cvt_pk_bf16_f32 v31, v32, v33
	v_cvt_pk_bf16_f32 v32, v26, v27
	v_cvt_pk_bf16_f32 v33, v28, v29
	v_add_u32_e32 v225, 0x80000, v226
	global_store_dwordx4 v225, v[30:33], s[4:5] offset:256
	s_waitcnt vmcnt(29)
	v_lshlrev_b32_e32 v170, 16, v202
	v_and_b32_e32 v202, 0xffff0000, v202
	v_lshlrev_b32_e32 v171, 16, v203
	v_and_b32_e32 v203, 0xffff0000, v203
	v_lshlrev_b32_e32 v214, 16, v204
	v_and_b32_e32 v204, 0xffff0000, v204
	v_lshlrev_b32_e32 v215, 16, v205
	v_and_b32_e32 v205, 0xffff0000, v205
	v_add_f32_e32 v170, v130, v170
	v_add_f32_e32 v202, v131, v202
	v_add_f32_e32 v171, v132, v171
	v_add_f32_e32 v203, v133, v203
	v_add_f32_e32 v214, v122, v214
	v_add_f32_e32 v204, v123, v204
	v_add_f32_e32 v215, v124, v215
	v_add_f32_e32 v205, v125, v205
	v_mul_f32_e32 v170, 0xbfb8aa3b, v170
	v_mul_f32_e32 v202, 0xbfb8aa3b, v202
	v_mul_f32_e32 v171, 0xbfb8aa3b, v171
	v_mul_f32_e32 v203, 0xbfb8aa3b, v203
	v_mul_f32_e32 v214, 0xbfb8aa3b, v214
	v_mul_f32_e32 v204, 0xbfb8aa3b, v204
	v_mul_f32_e32 v215, 0xbfb8aa3b, v215
	v_mul_f32_e32 v205, 0xbfb8aa3b, v205
	v_exp_f32_e32 v170, v170
	v_exp_f32_e32 v202, v202
	v_exp_f32_e32 v171, v171
	v_exp_f32_e32 v203, v203
	v_exp_f32_e32 v214, v214
	v_exp_f32_e32 v204, v204
	v_exp_f32_e32 v215, v215
	v_exp_f32_e32 v205, v205
	v_add_f32_e32 v170, 1.0, v170
	v_add_f32_e32 v202, 1.0, v202
	v_add_f32_e32 v171, 1.0, v171
	v_add_f32_e32 v203, 1.0, v203
	v_add_f32_e32 v214, 1.0, v214
	v_add_f32_e32 v204, 1.0, v204
	v_add_f32_e32 v215, 1.0, v215
	v_add_f32_e32 v205, 1.0, v205
	v_rcp_f32_e32 v170, v170
	v_rcp_f32_e32 v202, v202
	v_rcp_f32_e32 v171, v171
	v_rcp_f32_e32 v203, v203
	v_rcp_f32_e32 v214, v214
	v_rcp_f32_e32 v204, v204
	v_rcp_f32_e32 v215, v215
	v_rcp_f32_e32 v205, v205
	s_waitcnt vmcnt(6)
	v_lshlrev_b32_e32 v221, 16, v232
	v_and_b32_e32 v232, 0xffff0000, v232
	v_lshlrev_b32_e32 v222, 16, v233
	v_and_b32_e32 v233, 0xffff0000, v233
	v_lshlrev_b32_e32 v223, 16, v234
	v_and_b32_e32 v234, 0xffff0000, v234
	v_lshlrev_b32_e32 v224, 16, v235
	v_and_b32_e32 v235, 0xffff0000, v235
	v_fma_f32 v22, v22, v170, v221
	v_fma_f32 v23, v23, v202, v232
	v_fma_f32 v24, v24, v171, v222
	v_fma_f32 v25, v25, v203, v233
	v_fma_f32 v18, v18, v214, v223
	v_fma_f32 v19, v19, v204, v234
	v_fma_f32 v20, v20, v215, v224
	v_fma_f32 v21, v21, v205, v235
	v_cvt_pk_bf16_f32 v22, v22, v23
	v_cvt_pk_bf16_f32 v23, v24, v25
	v_cvt_pk_bf16_f32 v24, v18, v19
	v_cvt_pk_bf16_f32 v25, v20, v21
	v_add_u32_e32 v225, 0x90000, v226
	global_store_dwordx4 v225, v[22:25], s[4:5] offset:256
	s_waitcnt vmcnt(29)
; __device__ __forceinline__ v4u pack8(const float (&o)[8]) { v4u w; w.x = pk2(o[0], o[1]); w.y = pk2(o[2], o[3]); w.z = pk2(o[4], o[5]); w.w = pk2(o[6], o[7]); return w; }
; __device__ __forceinline__ float sigmf(float x) { return __builtin_amdgcn_rcpf(1.f + __expf(-x)); }
; __device__ __forceinline__ unsigned pk2(float lo, float hi) { typedef float f2v __attribute__((ext_vector_type(2))); typedef __bf16 b2v __attribute__((ext_vector_type(2))); const f2v v = {lo, hi}; return __builtin_bit_cast(unsigned, __builtin_convertvector(v, b2v)); }
; __device__ __forceinline__ void unpack8(const v4u w, float (&o)[8]) { o[0] = bflo(w.x); o[1] = bfhi(w.x); o[2] = bflo(w.y); o[3] = bfhi(w.y); o[4] = bflo(w.z); o[5] = bfhi(w.z); o[6] = bflo(w.w); o[7] = bfhi(w.w); }
;     __device__ __forceinline__ void operator()(const f32x4 (&acc)[2][2][4][2], const pg8::Unit& u, int wr, int wc, int fr, int fq_in) const {
;     ...
;                 for (int m = 0; m < 4; ++m) { const size_t row = (size_t)(row0 + ai * 128 + m * 16);
;                     gw_[m] = *(const v4u*)(Gt + row * (2 * D) + goff + col); pw_[m] = first ? (v4u){0u, 0u, 0u, 0u} : *(const v4u*)(O + row * D + col); }
;                 __builtin_amdgcn_sched_barrier(0);
; #pragma unroll
;                 for (int m = 0; m < 4; ++m) { const size_t row = (size_t)(row0 + ai * 128 + m * 16);
;                     float g0[8], p[8]; unpack8(gw_[m], g0); unpack8(pw_[m], p);
;                     float o[8];
; #pragma unroll
;                     for (int q = 0; q < 4; ++q) { o[q] = p[q] + sigmf(g0[q] + b0[q]) * acc[ai][bj][m][0][q]; o[4 + q] = p[4 + q] + sigmf(g0[4 + q] + b0[4 + q]) * acc[ai][bj][m][1][q]; }
;                     *(v4u*)(O + row * D + col) = pack8(o); }
	v_lshlrev_b32_e32 v170, 16, v206
	v_and_b32_e32 v206, 0xffff0000, v206
	v_lshlrev_b32_e32 v171, 16, v207
	v_and_b32_e32 v207, 0xffff0000, v207
	v_lshlrev_b32_e32 v214, 16, v208
	v_and_b32_e32 v208, 0xffff0000, v208
	v_lshlrev_b32_e32 v215, 16, v209
	v_and_b32_e32 v209, 0xffff0000, v209
	v_add_f32_e32 v170, v130, v170
	v_add_f32_e32 v206, v131, v206
	v_add_f32_e32 v171, v132, v171
	v_add_f32_e32 v207, v133, v207
	v_add_f32_e32 v214, v122, v214
	v_add_f32_e32 v208, v123, v208
	v_add_f32_e32 v215, v124, v215
	v_add_f32_e32 v209, v125, v209
	v_mul_f32_e32 v170, 0xbfb8aa3b, v170
	v_mul_f32_e32 v206, 0xbfb8aa3b, v206
	v_mul_f32_e32 v171, 0xbfb8aa3b, v171
	v_mul_f32_e32 v207, 0xbfb8aa3b, v207
	v_mul_f32_e32 v214, 0xbfb8aa3b, v214
	v_mul_f32_e32 v208, 0xbfb8aa3b, v208
	v_mul_f32_e32 v215, 0xbfb8aa3b, v215
	v_mul_f32_e32 v209, 0xbfb8aa3b, v209
	v_exp_f32_e32 v170, v170
	v_exp_f32_e32 v206, v206
	v_exp_f32_e32 v171, v171
	v_exp_f32_e32 v207, v207
	v_exp_f32_e32 v214, v214
	v_exp_f32_e32 v208, v208
	v_exp_f32_e32 v215, v215
	v_exp_f32_e32 v209, v209
	v_add_f32_e32 v170, 1.0, v170
	v_add_f32_e32 v206, 1.0, v206
	v_add_f32_e32 v171, 1.0, v171
	v_add_f32_e32 v207, 1.0, v207
	v_add_f32_e32 v214, 1.0, v214
	v_add_f32_e32 v208, 1.0, v208
	v_add_f32_e32 v215, 1.0, v215
	v_add_f32_e32 v209, 1.0, v209
	v_rcp_f32_e32 v170, v170
	v_rcp_f32_e32 v206, v206
	v_rcp_f32_e32 v171, v171
	v_rcp_f32_e32 v207, v207
	v_rcp_f32_e32 v214, v214
	v_rcp_f32_e32 v208, v208
	v_rcp_f32_e32 v215, v215
	v_rcp_f32_e32 v209, v209
	s_waitcnt vmcnt(5)
	v_lshlrev_b32_e32 v221, 16, v236
	v_and_b32_e32 v236, 0xffff0000, v236
	v_lshlrev_b32_e32 v222, 16, v237
	v_and_b32_e32 v237, 0xffff0000, v237
	v_lshlrev_b32_e32 v223, 16, v238
	v_and_b32_e32 v238, 0xffff0000, v238
	v_lshlrev_b32_e32 v224, 16, v239
	v_and_b32_e32 v239, 0xffff0000, v239
	v_fma_f32 v14, v14, v170, v221
	v_fma_f32 v15, v15, v206, v236
	v_fma_f32 v16, v16, v171, v222
	v_fma_f32 v17, v17, v207, v237
	v_fma_f32 v10, v10, v214, v223
	v_fma_f32 v11, v11, v208, v238
	v_fma_f32 v12, v12, v215, v224
	v_fma_f32 v13, v13, v209, v239
	v_cvt_pk_bf16_f32 v14, v14, v15
	v_cvt_pk_bf16_f32 v15, v16, v17
	v_cvt_pk_bf16_f32 v16, v10, v11
	v_cvt_pk_bf16_f32 v17, v12, v13
	v_add_u32_e32 v225, 0xa0000, v226
	global_store_dwordx4 v225, v[14:17], s[4:5] offset:256
	s_waitcnt vmcnt(29)
	v_lshlrev_b32_e32 v170, 16, v210
	v_and_b32_e32 v210, 0xffff0000, v210
	v_lshlrev_b32_e32 v171, 16, v211
	v_and_b32_e32 v211, 0xffff0000, v211
	v_lshlrev_b32_e32 v214, 16, v212
	v_and_b32_e32 v212, 0xffff0000, v212
	v_lshlrev_b32_e32 v215, 16, v213
	v_and_b32_e32 v213, 0xffff0000, v213
	v_add_f32_e32 v170, v130, v170
	v_add_f32_e32 v210, v131, v210
	v_add_f32_e32 v171, v132, v171
	v_add_f32_e32 v211, v133, v211
	v_add_f32_e32 v214, v122, v214
	v_add_f32_e32 v212, v123, v212
	v_add_f32_e32 v215, v124, v215
	v_add_f32_e32 v213, v125, v213
	v_mul_f32_e32 v170, 0xbfb8aa3b, v170
	v_mul_f32_e32 v210, 0xbfb8aa3b, v210
	v_mul_f32_e32 v171, 0xbfb8aa3b, v171
	v_mul_f32_e32 v211, 0xbfb8aa3b, v211
	v_mul_f32_e32 v214, 0xbfb8aa3b, v214
	v_mul_f32_e32 v212, 0xbfb8aa3b, v212
	v_mul_f32_e32 v215, 0xbfb8aa3b, v215
	v_mul_f32_e32 v213, 0xbfb8aa3b, v213
	v_exp_f32_e32 v170, v170
	v_exp_f32_e32 v210, v210
	v_exp_f32_e32 v171, v171
	v_exp_f32_e32 v211, v211
	v_exp_f32_e32 v214, v214
	v_exp_f32_e32 v212, v212
	v_exp_f32_e32 v215, v215
	v_exp_f32_e32 v213, v213
	v_add_f32_e32 v170, 1.0, v170
	v_add_f32_e32 v210, 1.0, v210
	v_add_f32_e32 v171, 1.0, v171
	v_add_f32_e32 v211, 1.0, v211
	v_add_f32_e32 v214, 1.0, v214
	v_add_f32_e32 v212, 1.0, v212
	v_add_f32_e32 v215, 1.0, v215
	v_add_f32_e32 v213, 1.0, v213
	v_rcp_f32_e32 v170, v170
	v_rcp_f32_e32 v210, v210
	v_rcp_f32_e32 v171, v171
	v_rcp_f32_e32 v211, v211
	v_rcp_f32_e32 v214, v214
	v_rcp_f32_e32 v212, v212
	v_rcp_f32_e32 v215, v215
	v_rcp_f32_e32 v213, v213
	s_waitcnt vmcnt(4)
	v_lshlrev_b32_e32 v221, 16, v240
	v_and_b32_e32 v240, 0xffff0000, v240
	v_lshlrev_b32_e32 v222, 16, v241
	v_and_b32_e32 v241, 0xffff0000, v241
	v_lshlrev_b32_e32 v223, 16, v242
	v_and_b32_e32 v242, 0xffff0000, v242
	v_lshlrev_b32_e32 v224, 16, v243
	v_and_b32_e32 v243, 0xffff0000, v243
	v_fma_f32 v6, v6, v170, v221
	v_fma_f32 v7, v7, v210, v240
	v_fma_f32 v8, v8, v171, v222
	v_fma_f32 v9, v9, v211, v241
	v_fma_f32 v2, v2, v214, v223
	v_fma_f32 v3, v3, v212, v242
	v_fma_f32 v4, v4, v215, v224
	v_fma_f32 v5, v5, v213, v243
	v_cvt_pk_bf16_f32 v6, v6, v7
	v_cvt_pk_bf16_f32 v7, v8, v9
	v_cvt_pk_bf16_f32 v8, v2, v3
	v_cvt_pk_bf16_f32 v9, v4, v5
	v_add_u32_e32 v225, 0xb0000, v226
	global_store_dwordx4 v225, v[6:9], s[4:5] offset:256
.Lepi6_done:
	s_andn2_b64 vcc, exec, s[24:25]
	s_mov_b64 s[8:9], -1
	s_cbranch_vccnz .LBB0_892
	s_andn2_b64 vcc, exec, s[2:3]
	s_cbranch_vccnz .LBB0_891
	s_barrier
	s_branch .LBB0_891

; __global__ void __launch_bounds__(NWAVES * 64, 2) mk_fwd(Args args) {
	.amdhsa_kernel _Z6mk_fwd4Args
		.amdhsa_group_segment_fixed_size 0
		.amdhsa_private_segment_fixed_size 0
		.amdhsa_kernarg_size 488
		.amdhsa_user_sgpr_count 2
		.amdhsa_user_sgpr_dispatch_ptr 0
		.amdhsa_user_sgpr_queue_ptr 0
		.amdhsa_user_sgpr_kernarg_segment_ptr 1
		.amdhsa_user_sgpr_dispatch_id 0
		.amdhsa_user_sgpr_kernarg_preload_length 0
		.amdhsa_user_sgpr_kernarg_preload_offset 0
		.amdhsa_user_sgpr_private_segment_size 0
		.amdhsa_uses_dynamic_stack 0
		.amdhsa_enable_private_segment 0
		.amdhsa_system_sgpr_workgroup_id_x 1
		.amdhsa_system_sgpr_workgroup_id_y 0
		.amdhsa_system_sgpr_workgroup_id_z 0
		.amdhsa_system_sgpr_workgroup_info 0
		.amdhsa_system_vgpr_workitem_id 0
		.amdhsa_next_free_vgpr 256
		.amdhsa_next_free_sgpr 102
		.amdhsa_accum_offset 256
		.amdhsa_reserve_vcc 1
		.amdhsa_float_round_mode_32 0
		.amdhsa_float_round_mode_16_64 0
		.amdhsa_float_denorm_mode_32 3
		.amdhsa_float_denorm_mode_16_64 3
		.amdhsa_dx10_clamp 1
		.amdhsa_ieee_mode 1
		.amdhsa_fp16_overflow 0
		.amdhsa_tg_split 0
		.amdhsa_exception_fp_ieee_invalid_op 0
		.amdhsa_exception_fp_denorm_src 0
		.amdhsa_exception_fp_ieee_div_zero 0
		.amdhsa_exception_fp_ieee_overflow 0
		.amdhsa_exception_fp_ieee_underflow 0
		.amdhsa_exception_fp_ieee_inexact 0
		.amdhsa_exception_int_div_zero 0
	.end_amdhsa_kernel

; __global__ void __launch_bounds__(NWAVES * 64, 2) mk_fwd(Args args) {
amdhsa.kernels:
  - .agpr_count:     0
    .args:
      - .offset:         0
        .size:           232
        .value_kind:     by_value
      - .offset:         232
        .size:           4
        .value_kind:     hidden_block_count_x
      - .offset:         236
        .size:           4
        .value_kind:     hidden_block_count_y
      - .offset:         240
        .size:           4
        .value_kind:     hidden_block_count_z
      - .offset:         244
        .size:           2
        .value_kind:     hidden_group_size_x
      - .offset:         246
        .size:           2
        .value_kind:     hidden_group_size_y
      - .offset:         248
        .size:           2
        .value_kind:     hidden_group_size_z
      - .offset:         250
        .size:           2
        .value_kind:     hidden_remainder_x
      - .offset:         252
        .size:           2
        .value_kind:     hidden_remainder_y
      - .offset:         254
        .size:           2
        .value_kind:     hidden_remainder_z
      - .offset:         272
        .size:           8
        .value_kind:     hidden_global_offset_x
      - .offset:         280
        .size:           8
        .value_kind:     hidden_global_offset_y
      - .offset:         288
        .size:           8
        .value_kind:     hidden_global_offset_z
      - .offset:         296
        .size:           2
        .value_kind:     hidden_grid_dims
      - .offset:         352
        .size:           4
        .value_kind:     hidden_dynamic_lds_size
    .group_segment_fixed_size: 0
    .kernarg_segment_align: 8
    .kernarg_segment_size: 488
    .language:       OpenCL C
    .language_version:
      - 2
      - 0
    .max_flat_workgroup_size: 512
    .name:           _Z6mk_fwd4Args
    .private_segment_fixed_size: 0
    .sgpr_count:     108
    .sgpr_spill_count: 69
    .symbol:         _Z6mk_fwd4Args.kd
    .uniform_work_group_size: 1
    .uses_dynamic_stack: false
    .vgpr_count:     256
    .vgpr_spill_count: 0
    .wavefront_size: 64
